# baseline (speedup 1.0000x reference)
.LBB6_12:
	ds_read_b128 v[176:179], v169
	ds_read_b128 v[180:183], v170
	ds_read_b128 v[184:187], v171
	ds_read_b128 v[188:191], v172
	v_add_u32_e32 v174, 0xc000, v152
	v_lshl_add_u64 v[192:193], v[136:137], 0, s[44:45]
	v_add_u32_e32 v175, 0xe000, v152
	v_add_u32_e32 v173, s17, v168
	ds_read_b128 v[196:199], v173
	ds_read_b128 v[200:203], v173 offset:1024
	ds_read_b128 v[204:207], v173 offset:2048
	ds_read_b128 v[212:215], v173 offset:3072
	ds_read_b128 v[216:219], v173 offset:4096
	ds_read_b128 v[220:223], v173 offset:5120
	ds_read_b128 v[224:227], v173 offset:6144
	ds_read_b128 v[228:231], v173 offset:7168
	v_lshl_add_u64 v[232:233], v[192:193], 0, s[30:31]
	s_mov_b32 m0, s72
	v_lshl_add_u64 v[248:249], v[134:135], 0, s[44:45]
	global_load_lds_dwordx4 v[232:233], off
	s_mov_b32 m0, s73
	v_lshl_add_u64 v[232:233], v[248:249], 0, s[30:31]
	global_load_lds_dwordx4 v[232:233], off
	s_waitcnt lgkmcnt(8)
	s_barrier
	s_waitcnt lgkmcnt(0)
	v_mfma_f32_16x16x32_f16 v[2:5], v[196:199], v[176:179], v[2:5]
	v_mfma_f32_16x16x32_f16 v[6:9], v[196:199], v[184:187], v[6:9]
	v_mfma_f32_16x16x32_f16 v[10:13], v[204:207], v[176:179], v[10:13]
	v_mfma_f32_16x16x32_f16 v[18:21], v[204:207], v[184:187], v[18:21]
	v_mfma_f32_16x16x32_f16 v[30:33], v[216:219], v[176:179], v[30:33]
	v_mfma_f32_16x16x32_f16 v[42:45], v[216:219], v[184:187], v[42:45]
	v_mfma_f32_16x16x32_f16 v[54:57], v[224:227], v[176:179], v[54:57]
	v_mfma_f32_16x16x32_f16 v[66:69], v[224:227], v[184:187], v[66:69]
	v_mfma_f32_16x16x32_f16 v[2:5], v[200:203], v[180:183], v[2:5]
	v_mfma_f32_16x16x32_f16 v[6:9], v[200:203], v[188:191], v[6:9]
	v_mfma_f32_16x16x32_f16 v[10:13], v[212:215], v[180:183], v[10:13]
	v_mfma_f32_16x16x32_f16 v[18:21], v[212:215], v[188:191], v[18:21]
	v_mfma_f32_16x16x32_f16 v[30:33], v[220:223], v[180:183], v[30:33]
	v_mfma_f32_16x16x32_f16 v[42:45], v[220:223], v[188:191], v[42:45]
	v_mfma_f32_16x16x32_f16 v[54:57], v[228:231], v[180:183], v[54:57]
	v_mfma_f32_16x16x32_f16 v[66:69], v[228:231], v[188:191], v[66:69]
	s_barrier
	v_lshl_add_u64 v[250:251], v[140:141], 0, s[44:45]
	v_lshl_add_u64 v[252:253], v[250:251], 0, s[34:35]
	s_mov_b32 m0, s74
	ds_read_b128 v[232:235], v161
	ds_read_b128 v[236:239], v162
	ds_read_b128 v[240:243], v163
	ds_read_b128 v[244:247], v164
	global_load_lds_dwordx4 v[252:253], off
	v_lshl_add_u64 v[252:253], v[138:139], 0, s[44:45]
	s_mov_b32 m0, s75
	v_lshl_add_u64 v[254:255], v[252:253], 0, s[34:35]
	global_load_lds_dwordx4 v[254:255], off
	s_barrier
	s_waitcnt lgkmcnt(0)
	v_mfma_f32_16x16x32_f16 v[14:17], v[196:199], v[232:235], v[14:17]
	v_mfma_f32_16x16x32_f16 v[22:25], v[196:199], v[240:243], v[22:25]
	v_mfma_f32_16x16x32_f16 v[34:37], v[204:207], v[232:235], v[34:37]
	v_mfma_f32_16x16x32_f16 v[46:49], v[204:207], v[240:243], v[46:49]
	v_mfma_f32_16x16x32_f16 v[58:61], v[216:219], v[232:235], v[58:61]
	v_mfma_f32_16x16x32_f16 v[70:73], v[216:219], v[240:243], v[70:73]
	v_mfma_f32_16x16x32_f16 v[78:81], v[224:227], v[232:235], v[78:81]
	v_mfma_f32_16x16x32_f16 v[86:89], v[224:227], v[240:243], v[86:89]
	v_mfma_f32_16x16x32_f16 v[14:17], v[200:203], v[236:239], v[14:17]
	v_mfma_f32_16x16x32_f16 v[22:25], v[200:203], v[244:247], v[22:25]
	v_mfma_f32_16x16x32_f16 v[34:37], v[212:215], v[236:239], v[34:37]
	v_mfma_f32_16x16x32_f16 v[46:49], v[212:215], v[244:247], v[46:49]
	v_mfma_f32_16x16x32_f16 v[58:61], v[220:223], v[236:239], v[58:61]
	v_mfma_f32_16x16x32_f16 v[70:73], v[220:223], v[244:247], v[70:73]
	v_mfma_f32_16x16x32_f16 v[78:81], v[228:231], v[236:239], v[78:81]
	v_mfma_f32_16x16x32_f16 v[86:89], v[228:231], v[244:247], v[86:89]
	v_lshl_add_u64 v[254:255], v[192:193], 0, s[34:35]
	s_mov_b32 m0, s76
	s_barrier
	ds_read_b128 v[196:199], v173 offset:16384
	ds_read_b128 v[200:203], v173 offset:17408
	ds_read_b128 v[204:207], v173 offset:18432
	ds_read_b128 v[212:215], v173 offset:19456
	ds_read_b128 v[216:219], v173 offset:20480
	ds_read_b128 v[220:223], v173 offset:21504
	ds_read_b128 v[224:227], v173 offset:22528
	ds_read_b128 v[228:231], v173 offset:23552
	global_load_lds_dwordx4 v[254:255], off
	s_mov_b32 m0, s77
	v_lshl_add_u64 v[254:255], v[248:249], 0, s[34:35]
	global_load_lds_dwordx4 v[254:255], off
	s_barrier
	s_waitcnt lgkmcnt(0)
	v_mfma_f32_16x16x32_f16 v[26:29], v[196:199], v[176:179], v[26:29]
	v_mfma_f32_16x16x32_f16 v[38:41], v[196:199], v[184:187], v[38:41]
	v_mfma_f32_16x16x32_f16 v[50:53], v[204:207], v[176:179], v[50:53]
	v_mfma_f32_16x16x32_f16 v[62:65], v[204:207], v[184:187], v[62:65]
	v_mfma_f32_16x16x32_f16 v[74:77], v[216:219], v[176:179], v[74:77]
	v_mfma_f32_16x16x32_f16 v[82:85], v[216:219], v[184:187], v[82:85]
	v_mfma_f32_16x16x32_f16 v[90:93], v[224:227], v[176:179], v[90:93]
	v_mfma_f32_16x16x32_f16 v[94:97], v[224:227], v[184:187], v[94:97]
	v_mfma_f32_16x16x32_f16 v[26:29], v[200:203], v[180:183], v[26:29]
	v_mfma_f32_16x16x32_f16 v[38:41], v[200:203], v[188:191], v[38:41]
	v_mfma_f32_16x16x32_f16 v[50:53], v[212:215], v[180:183], v[50:53]
	v_mfma_f32_16x16x32_f16 v[62:65], v[212:215], v[188:191], v[62:65]
	v_mfma_f32_16x16x32_f16 v[74:77], v[220:223], v[180:183], v[74:77]
	v_mfma_f32_16x16x32_f16 v[82:85], v[220:223], v[188:191], v[82:85]
	v_mfma_f32_16x16x32_f16 v[90:93], v[228:231], v[180:183], v[90:93]
	v_mfma_f32_16x16x32_f16 v[94:97], v[228:231], v[188:191], v[94:97]
	s_barrier
	s_mov_b32 m0, s78
	v_lshl_add_u64 v[176:177], v[250:251], 0, s[36:37]
	global_load_lds_dwordx4 v[176:177], off
	s_mov_b32 m0, s79
	v_lshl_add_u64 v[176:177], v[252:253], 0, s[36:37]
	global_load_lds_dwordx4 v[176:177], off
	s_waitcnt vmcnt(6)
	s_barrier
	v_mfma_f32_16x16x32_f16 v[98:101], v[196:199], v[232:235], v[98:101]
	v_mfma_f32_16x16x32_f16 v[102:105], v[196:199], v[240:243], v[102:105]
	v_mfma_f32_16x16x32_f16 v[106:109], v[204:207], v[232:235], v[106:109]
	v_mfma_f32_16x16x32_f16 v[110:113], v[204:207], v[240:243], v[110:113]
	v_mfma_f32_16x16x32_f16 v[114:117], v[216:219], v[232:235], v[114:117]
	v_mfma_f32_16x16x32_f16 v[118:121], v[216:219], v[240:243], v[118:121]
	v_mfma_f32_16x16x32_f16 v[122:125], v[224:227], v[232:235], v[122:125]
	v_mfma_f32_16x16x32_f16 v[126:129], v[224:227], v[240:243], v[126:129]
	v_mfma_f32_16x16x32_f16 v[98:101], v[200:203], v[236:239], v[98:101]
	v_mfma_f32_16x16x32_f16 v[102:105], v[200:203], v[244:247], v[102:105]
	v_mfma_f32_16x16x32_f16 v[106:109], v[212:215], v[236:239], v[106:109]
	v_mfma_f32_16x16x32_f16 v[110:113], v[212:215], v[244:247], v[110:113]
	v_mfma_f32_16x16x32_f16 v[114:117], v[220:223], v[236:239], v[114:117]
	v_mfma_f32_16x16x32_f16 v[118:121], v[220:223], v[244:247], v[118:121]
	v_mfma_f32_16x16x32_f16 v[122:125], v[228:231], v[236:239], v[122:125]
	v_mfma_f32_16x16x32_f16 v[126:129], v[228:231], v[244:247], v[126:129]
	s_barrier
	ds_read_b128 v[176:179], v148
	ds_read_b128 v[180:183], v149
	ds_read_b128 v[184:187], v150
	ds_read_b128 v[188:191], v151
	ds_read_b128 v[196:199], v173 offset:32768
	ds_read_b128 v[200:203], v173 offset:33792
	ds_read_b128 v[204:207], v173 offset:34816
	ds_read_b128 v[212:215], v173 offset:35840
	ds_read_b128 v[216:219], v173 offset:36864
	ds_read_b128 v[220:223], v173 offset:37888
	ds_read_b128 v[224:227], v173 offset:38912
	ds_read_b128 v[228:231], v173 offset:39936
	s_mov_b32 m0, s80
	v_lshl_add_u64 v[232:233], v[192:193], 0, s[36:37]
	global_load_lds_dwordx4 v[232:233], off
	s_mov_b32 m0, s81
	v_lshl_add_u64 v[232:233], v[248:249], 0, s[36:37]
	global_load_lds_dwordx4 v[232:233], off
	s_waitcnt lgkmcnt(8)
	s_barrier
	s_waitcnt lgkmcnt(0)
	v_mfma_f32_16x16x32_f16 v[2:5], v[196:199], v[176:179], v[2:5]
	v_mfma_f32_16x16x32_f16 v[6:9], v[196:199], v[184:187], v[6:9]
	v_mfma_f32_16x16x32_f16 v[10:13], v[204:207], v[176:179], v[10:13]
	v_mfma_f32_16x16x32_f16 v[18:21], v[204:207], v[184:187], v[18:21]
	v_mfma_f32_16x16x32_f16 v[30:33], v[216:219], v[176:179], v[30:33]
	v_mfma_f32_16x16x32_f16 v[42:45], v[216:219], v[184:187], v[42:45]
	v_mfma_f32_16x16x32_f16 v[54:57], v[224:227], v[176:179], v[54:57]
	v_mfma_f32_16x16x32_f16 v[66:69], v[224:227], v[184:187], v[66:69]
	v_mfma_f32_16x16x32_f16 v[2:5], v[200:203], v[180:183], v[2:5]
	v_mfma_f32_16x16x32_f16 v[6:9], v[200:203], v[188:191], v[6:9]
	v_mfma_f32_16x16x32_f16 v[10:13], v[212:215], v[180:183], v[10:13]
	v_mfma_f32_16x16x32_f16 v[18:21], v[212:215], v[188:191], v[18:21]
	v_mfma_f32_16x16x32_f16 v[30:33], v[220:223], v[180:183], v[30:33]
	v_mfma_f32_16x16x32_f16 v[42:45], v[220:223], v[188:191], v[42:45]
	v_mfma_f32_16x16x32_f16 v[54:57], v[228:231], v[180:183], v[54:57]
	v_mfma_f32_16x16x32_f16 v[66:69], v[228:231], v[188:191], v[66:69]
	s_barrier
	v_lshl_add_u64 v[254:255], v[250:251], 0, s[38:39]
	s_mov_b32 m0, s82
	ds_read_b128 v[232:235], v142
	ds_read_b128 v[236:239], v143
	ds_read_b128 v[240:243], v144
	ds_read_b128 v[244:247], v145
	global_load_lds_dwordx4 v[254:255], off
	s_mov_b32 m0, s83
	v_lshl_add_u64 v[254:255], v[252:253], 0, s[38:39]
	global_load_lds_dwordx4 v[254:255], off
	s_barrier
	s_waitcnt lgkmcnt(0)
	v_mfma_f32_16x16x32_f16 v[14:17], v[196:199], v[232:235], v[14:17]
	v_mfma_f32_16x16x32_f16 v[22:25], v[196:199], v[240:243], v[22:25]
	v_mfma_f32_16x16x32_f16 v[34:37], v[204:207], v[232:235], v[34:37]
	v_mfma_f32_16x16x32_f16 v[46:49], v[204:207], v[240:243], v[46:49]
	v_mfma_f32_16x16x32_f16 v[58:61], v[216:219], v[232:235], v[58:61]
	v_mfma_f32_16x16x32_f16 v[70:73], v[216:219], v[240:243], v[70:73]
	v_mfma_f32_16x16x32_f16 v[78:81], v[224:227], v[232:235], v[78:81]
	v_mfma_f32_16x16x32_f16 v[86:89], v[224:227], v[240:243], v[86:89]
	v_mfma_f32_16x16x32_f16 v[14:17], v[200:203], v[236:239], v[14:17]
	v_mfma_f32_16x16x32_f16 v[22:25], v[200:203], v[244:247], v[22:25]
	v_mfma_f32_16x16x32_f16 v[34:37], v[212:215], v[236:239], v[34:37]
	v_mfma_f32_16x16x32_f16 v[46:49], v[212:215], v[244:247], v[46:49]
	v_mfma_f32_16x16x32_f16 v[58:61], v[220:223], v[236:239], v[58:61]
	v_mfma_f32_16x16x32_f16 v[70:73], v[220:223], v[244:247], v[70:73]
	v_mfma_f32_16x16x32_f16 v[78:81], v[228:231], v[236:239], v[78:81]
	v_mfma_f32_16x16x32_f16 v[86:89], v[228:231], v[244:247], v[86:89]
	v_lshl_add_u64 v[192:193], v[192:193], 0, s[38:39]
	s_mov_b32 m0, s84
	s_barrier
	ds_read_b128 v[196:199], v173 offset:49152
	ds_read_b128 v[200:203], v173 offset:50176
	ds_read_b128 v[204:207], v173 offset:51200
	ds_read_b128 v[212:215], v173 offset:52224
	ds_read_b128 v[216:219], v173 offset:53248
	ds_read_b128 v[220:223], v173 offset:54272
	ds_read_b128 v[224:227], v173 offset:55296
	ds_read_b128 v[228:231], v173 offset:56320
	global_load_lds_dwordx4 v[192:193], off
	s_mov_b32 m0, s85
	v_lshl_add_u64 v[192:193], v[248:249], 0, s[38:39]
	global_load_lds_dwordx4 v[192:193], off
	s_barrier
	s_waitcnt lgkmcnt(0)
	v_mfma_f32_16x16x32_f16 v[26:29], v[196:199], v[176:179], v[26:29]
	v_mfma_f32_16x16x32_f16 v[38:41], v[196:199], v[184:187], v[38:41]
	v_mfma_f32_16x16x32_f16 v[50:53], v[204:207], v[176:179], v[50:53]
	v_mfma_f32_16x16x32_f16 v[62:65], v[204:207], v[184:187], v[62:65]
	v_mfma_f32_16x16x32_f16 v[74:77], v[216:219], v[176:179], v[74:77]
	v_mfma_f32_16x16x32_f16 v[82:85], v[216:219], v[184:187], v[82:85]
	v_mfma_f32_16x16x32_f16 v[90:93], v[224:227], v[176:179], v[90:93]
	v_mfma_f32_16x16x32_f16 v[94:97], v[224:227], v[184:187], v[94:97]
	v_mfma_f32_16x16x32_f16 v[26:29], v[200:203], v[180:183], v[26:29]
	v_mfma_f32_16x16x32_f16 v[38:41], v[200:203], v[188:191], v[38:41]
	v_mfma_f32_16x16x32_f16 v[50:53], v[212:215], v[180:183], v[50:53]
	v_mfma_f32_16x16x32_f16 v[62:65], v[212:215], v[188:191], v[62:65]
	v_mfma_f32_16x16x32_f16 v[74:77], v[220:223], v[180:183], v[74:77]
	v_mfma_f32_16x16x32_f16 v[82:85], v[220:223], v[188:191], v[82:85]
	v_mfma_f32_16x16x32_f16 v[90:93], v[228:231], v[180:183], v[90:93]
	v_mfma_f32_16x16x32_f16 v[94:97], v[228:231], v[188:191], v[94:97]
	s_barrier
	s_mov_b32 m0, s86
	v_lshl_add_u64 v[176:177], v[250:251], 0, s[40:41]
	global_load_lds_dwordx4 v[176:177], off
	s_mov_b32 m0, s87
	v_lshl_add_u64 v[176:177], v[252:253], 0, s[40:41]
	global_load_lds_dwordx4 v[176:177], off
	s_waitcnt vmcnt(6)
	s_barrier
	v_mfma_f32_16x16x32_f16 v[98:101], v[196:199], v[232:235], v[98:101]
	v_mfma_f32_16x16x32_f16 v[102:105], v[196:199], v[240:243], v[102:105]
	v_mfma_f32_16x16x32_f16 v[106:109], v[204:207], v[232:235], v[106:109]
	v_mfma_f32_16x16x32_f16 v[110:113], v[204:207], v[240:243], v[110:113]
	v_mfma_f32_16x16x32_f16 v[114:117], v[216:219], v[232:235], v[114:117]
	v_mfma_f32_16x16x32_f16 v[118:121], v[216:219], v[240:243], v[118:121]
	v_mfma_f32_16x16x32_f16 v[122:125], v[224:227], v[232:235], v[122:125]
	v_mfma_f32_16x16x32_f16 v[126:129], v[224:227], v[240:243], v[126:129]
	v_mfma_f32_16x16x32_f16 v[98:101], v[200:203], v[236:239], v[98:101]
	v_mfma_f32_16x16x32_f16 v[102:105], v[200:203], v[244:247], v[102:105]
	v_mfma_f32_16x16x32_f16 v[106:109], v[212:215], v[236:239], v[106:109]
	v_mfma_f32_16x16x32_f16 v[110:113], v[212:215], v[244:247], v[110:113]
	v_mfma_f32_16x16x32_f16 v[114:117], v[220:223], v[236:239], v[114:117]
	v_mfma_f32_16x16x32_f16 v[118:121], v[220:223], v[244:247], v[118:121]
	v_mfma_f32_16x16x32_f16 v[122:125], v[228:231], v[236:239], v[122:125]
	v_mfma_f32_16x16x32_f16 v[126:129], v[228:231], v[244:247], v[126:129]
	s_add_i32 s46, s46, 2
	s_add_u32 s44, s44, 0x100
	s_addc_u32 s45, s45, 0
	s_cmp_lt_u32 s46, 4
	s_barrier
	s_cbranch_scc1 .LBB6_12
	s_add_u32 s0, s0, 0x20380
	s_addc_u32 s1, s1, 0
	v_readfirstlane_b32 s17, v174
	v_lshl_add_u64 v[130:131], v[130:131], 1, s[0:1]
	s_mov_b32 m0, s17
	ds_read_b128 v[134:137], v169
	ds_read_b128 v[138:141], v170
	ds_read_b128 v[152:155], v171
	ds_read_b128 v[156:159], v172
	ds_read_b128 v[166:169], v173
	ds_read_b128 v[176:179], v173 offset:1024
	ds_read_b128 v[180:183], v173 offset:2048
	ds_read_b128 v[184:187], v173 offset:3072
	ds_read_b128 v[188:191], v173 offset:4096
	ds_read_b128 v[196:199], v173 offset:5120
	ds_read_b128 v[200:203], v173 offset:6144
	ds_read_b128 v[204:207], v173 offset:7168
	global_load_lds_dwordx4 v[130:131], off
	v_lshl_add_u64 v[130:131], v[132:133], 1, s[0:1]
	v_readfirstlane_b32 s0, v175
	s_mov_b32 m0, s0
	s_nop 0
	global_load_lds_dwordx4 v[130:131], off
	s_barrier
	s_waitcnt lgkmcnt(0)
	v_mfma_f32_16x16x32_f16 v[2:5], v[166:169], v[134:137], v[2:5]
	v_mfma_f32_16x16x32_f16 v[42:45], v[188:191], v[152:155], v[42:45]
	v_mfma_f32_16x16x32_f16 v[54:57], v[200:203], v[134:137], v[54:57]
	v_mfma_f32_16x16x32_f16 v[66:69], v[200:203], v[152:155], v[66:69]
	v_mfma_f32_16x16x32_f16 v[2:5], v[176:179], v[138:141], v[2:5]
	v_mfma_f32_16x16x32_f16 v[6:9], v[166:169], v[152:155], v[6:9]
	v_mfma_f32_16x16x32_f16 v[10:13], v[180:183], v[134:137], v[10:13]
	v_mfma_f32_16x16x32_f16 v[18:21], v[180:183], v[152:155], v[18:21]
	v_mfma_f32_16x16x32_f16 v[30:33], v[188:191], v[134:137], v[30:33]
	v_mfma_f32_16x16x32_f16 v[42:45], v[196:199], v[156:159], v[42:45]
	v_mfma_f32_16x16x32_f16 v[54:57], v[204:207], v[138:141], v[54:57]
	v_mfma_f32_16x16x32_f16 v[66:69], v[204:207], v[156:159], v[66:69]
	v_mfma_f32_16x16x32_f16 v[6:9], v[176:179], v[156:159], v[6:9]
	v_mfma_f32_16x16x32_f16 v[10:13], v[184:187], v[138:141], v[10:13]
	v_mfma_f32_16x16x32_f16 v[18:21], v[184:187], v[156:159], v[18:21]
	v_mfma_f32_16x16x32_f16 v[30:33], v[196:199], v[138:141], v[30:33]
	s_barrier
	ds_read_b128 v[130:133], v161
	ds_read_b128 v[212:215], v162
	ds_read_b128 v[160:163], v163
	ds_read_b128 v[216:219], v164
	s_barrier
	s_waitcnt lgkmcnt(0)
	v_mfma_f32_16x16x32_f16 v[14:17], v[166:169], v[130:133], v[14:17]
	v_mfma_f32_16x16x32_f16 v[78:81], v[200:203], v[130:133], v[78:81]
	v_mfma_f32_16x16x32_f16 v[14:17], v[176:179], v[212:215], v[14:17]
	v_mfma_f32_16x16x32_f16 v[22:25], v[166:169], v[160:163], v[22:25]
	v_mfma_f32_16x16x32_f16 v[34:37], v[180:183], v[130:133], v[34:37]
	v_mfma_f32_16x16x32_f16 v[46:49], v[180:183], v[160:163], v[46:49]
	v_mfma_f32_16x16x32_f16 v[58:61], v[188:191], v[130:133], v[58:61]
	v_mfma_f32_16x16x32_f16 v[70:73], v[188:191], v[160:163], v[70:73]
	v_mfma_f32_16x16x32_f16 v[164:167], v[204:207], v[212:215], v[78:81]
	v_mfma_f32_16x16x32_f16 v[78:81], v[200:203], v[160:163], v[86:89]
	v_mfma_f32_16x16x32_f16 v[22:25], v[176:179], v[216:219], v[22:25]
	v_mfma_f32_16x16x32_f16 v[34:37], v[184:187], v[212:215], v[34:37]
	v_mfma_f32_16x16x32_f16 v[46:49], v[184:187], v[216:219], v[46:49]
	v_mfma_f32_16x16x32_f16 v[58:61], v[196:199], v[212:215], v[58:61]
	v_mfma_f32_16x16x32_f16 v[70:73], v[196:199], v[216:219], v[70:73]
	v_mfma_f32_16x16x32_f16 v[86:89], v[204:207], v[216:219], v[78:81]
	s_barrier
	s_nop 0
	ds_read_b128 v[78:81], v173 offset:16384
	ds_read_b128 v[168:171], v173 offset:17408
	ds_read_b128 v[174:177], v173 offset:18432
	ds_read_b128 v[178:181], v173 offset:19456
	ds_read_b128 v[182:185], v173 offset:20480
	ds_read_b128 v[186:189], v173 offset:21504
	ds_read_b128 v[190:193], v173 offset:22528
	ds_read_b128 v[196:199], v173 offset:23552
	s_waitcnt vmcnt(4)
	s_barrier
	s_waitcnt lgkmcnt(0)
	v_mfma_f32_16x16x32_f16 v[26:29], v[78:81], v[134:137], v[26:29]
	v_mfma_f32_16x16x32_f16 v[38:41], v[78:81], v[152:155], v[38:41]
	v_mfma_f32_16x16x32_f16 v[26:29], v[168:171], v[138:141], v[26:29]
	v_mfma_f32_16x16x32_f16 v[38:41], v[168:171], v[156:159], v[38:41]
	v_mfma_f32_16x16x32_f16 v[50:53], v[174:177], v[134:137], v[50:53]
	v_mfma_f32_16x16x32_f16 v[62:65], v[174:177], v[152:155], v[62:65]
	v_mfma_f32_16x16x32_f16 v[74:77], v[182:185], v[134:137], v[74:77]
	v_mfma_f32_16x16x32_f16 v[82:85], v[182:185], v[152:155], v[82:85]
	v_mfma_f32_16x16x32_f16 v[90:93], v[190:193], v[134:137], v[90:93]
	v_mfma_f32_16x16x32_f16 v[94:97], v[190:193], v[152:155], v[94:97]
	v_mfma_f32_16x16x32_f16 v[50:53], v[178:181], v[138:141], v[50:53]
	v_mfma_f32_16x16x32_f16 v[62:65], v[178:181], v[156:159], v[62:65]
	v_mfma_f32_16x16x32_f16 v[74:77], v[186:189], v[138:141], v[74:77]
	v_mfma_f32_16x16x32_f16 v[82:85], v[186:189], v[156:159], v[82:85]
	v_mfma_f32_16x16x32_f16 v[90:93], v[196:199], v[138:141], v[90:93]
	v_mfma_f32_16x16x32_f16 v[94:97], v[196:199], v[156:159], v[94:97]
	v_mfma_f32_16x16x32_f16 v[98:101], v[78:81], v[130:133], v[98:101]
	v_mfma_f32_16x16x32_f16 v[78:81], v[78:81], v[160:163], v[102:105]
	v_mfma_f32_16x16x32_f16 v[102:105], v[168:171], v[216:219], v[78:81]
	v_mfma_f32_16x16x32_f16 v[78:81], v[174:177], v[130:133], v[106:109]
	v_mfma_f32_16x16x32_f16 v[106:109], v[178:181], v[212:215], v[78:81]
	v_mfma_f32_16x16x32_f16 v[78:81], v[174:177], v[160:163], v[110:113]
	v_mfma_f32_16x16x32_f16 v[200:203], v[178:181], v[216:219], v[78:81]
	v_mfma_f32_16x16x32_f16 v[78:81], v[182:185], v[130:133], v[114:117]
	v_mfma_f32_16x16x32_f16 v[204:207], v[186:189], v[212:215], v[78:81]
	v_mfma_f32_16x16x32_f16 v[78:81], v[182:185], v[160:163], v[118:121]
	v_mfma_f32_16x16x32_f16 v[220:223], v[186:189], v[216:219], v[78:81]
	v_mfma_f32_16x16x32_f16 v[78:81], v[190:193], v[130:133], v[122:125]
	v_mfma_f32_16x16x32_f16 v[98:101], v[168:171], v[212:215], v[98:101]
	v_mfma_f32_16x16x32_f16 v[212:215], v[196:199], v[212:215], v[78:81]
	v_mfma_f32_16x16x32_f16 v[78:81], v[190:193], v[160:163], v[126:129]
	v_mfma_f32_16x16x32_f16 v[196:199], v[196:199], v[216:219], v[78:81]
	s_barrier
	ds_read_b128 v[110:113], v148
	ds_read_b128 v[130:133], v149
	ds_read_b128 v[216:219], v150
	ds_read_b128 v[224:227], v151
	s_nop 0
	ds_read_b128 v[78:81], v173 offset:32768
	ds_read_b128 v[114:117], v173 offset:33792
	ds_read_b128 v[118:121], v173 offset:34816
	ds_read_b128 v[134:137], v173 offset:35840
	ds_read_b128 v[138:141], v173 offset:36864
	ds_read_b128 v[168:171], v173 offset:37888
	ds_read_b128 v[174:177], v173 offset:38912
	ds_read_b128 v[228:231], v173 offset:39936
	s_waitcnt vmcnt(2)
	s_barrier
	s_waitcnt lgkmcnt(0)
	v_mfma_f32_16x16x32_f16 v[2:5], v[78:81], v[110:113], v[2:5]
	v_mfma_f32_16x16x32_f16 v[190:193], v[114:117], v[130:133], v[2:5]
	v_mfma_f32_16x16x32_f16 v[2:5], v[78:81], v[216:219], v[6:9]
	v_mfma_f32_16x16x32_f16 v[158:161], v[114:117], v[224:227], v[2:5]
	v_mfma_f32_16x16x32_f16 v[2:5], v[118:121], v[110:113], v[10:13]
	v_mfma_f32_16x16x32_f16 v[186:189], v[134:137], v[130:133], v[2:5]
	v_mfma_f32_16x16x32_f16 v[2:5], v[118:121], v[216:219], v[18:21]
	v_mfma_f32_16x16x32_f16 v[154:157], v[134:137], v[224:227], v[2:5]
	v_mfma_f32_16x16x32_f16 v[2:5], v[138:141], v[110:113], v[30:33]
	v_mfma_f32_16x16x32_f16 v[182:185], v[168:171], v[130:133], v[2:5]
	v_mfma_f32_16x16x32_f16 v[2:5], v[138:141], v[216:219], v[42:45]
	v_mfma_f32_16x16x32_f16 v[150:153], v[168:171], v[224:227], v[2:5]
	v_mfma_f32_16x16x32_f16 v[2:5], v[174:177], v[110:113], v[54:57]
	v_mfma_f32_16x16x32_f16 v[178:181], v[228:231], v[130:133], v[2:5]
	v_mfma_f32_16x16x32_f16 v[2:5], v[174:177], v[216:219], v[66:69]
	v_mfma_f32_16x16x32_f16 v[146:149], v[228:231], v[224:227], v[2:5]
	s_barrier
	s_nop 4
	ds_read_b128 v[2:5], v142
	ds_read_b128 v[6:9], v143
	ds_read_b128 v[10:13], v144
	ds_read_b128 v[18:21], v145
	s_waitcnt vmcnt(0)
	s_barrier
	s_waitcnt lgkmcnt(0)
	v_mfma_f32_16x16x32_f16 v[14:17], v[78:81], v[2:5], v[14:17]
	v_mfma_f32_16x16x32_f16 v[126:129], v[114:117], v[6:9], v[14:17]
	v_mfma_f32_16x16x32_f16 v[14:17], v[78:81], v[10:13], v[22:25]
	v_mfma_f32_16x16x32_f16 v[78:81], v[114:117], v[18:21], v[14:17]
	v_mfma_f32_16x16x32_f16 v[14:17], v[118:121], v[2:5], v[34:37]
	v_mfma_f32_16x16x32_f16 v[122:125], v[134:137], v[6:9], v[14:17]
	v_mfma_f32_16x16x32_f16 v[14:17], v[118:121], v[10:13], v[46:49]
	v_mfma_f32_16x16x32_f16 v[66:69], v[134:137], v[18:21], v[14:17]
	v_mfma_f32_16x16x32_f16 v[14:17], v[138:141], v[2:5], v[58:61]
	v_mfma_f32_16x16x32_f16 v[118:121], v[168:171], v[6:9], v[14:17]
	v_mfma_f32_16x16x32_f16 v[14:17], v[138:141], v[10:13], v[70:73]
	v_mfma_f32_16x16x32_f16 v[54:57], v[168:171], v[18:21], v[14:17]
	v_mfma_f32_16x16x32_f16 v[14:17], v[174:177], v[2:5], v[164:167]
	v_mfma_f32_16x16x32_f16 v[114:117], v[228:231], v[6:9], v[14:17]
	v_mfma_f32_16x16x32_f16 v[14:17], v[174:177], v[10:13], v[86:89]
	v_mfma_f32_16x16x32_f16 v[42:45], v[228:231], v[18:21], v[14:17]
	s_barrier
	s_nop 4
	ds_read_b128 v[14:17], v173 offset:49152
	ds_read_b128 v[22:25], v173 offset:50176
	ds_read_b128 v[30:33], v173 offset:51200
	ds_read_b128 v[34:37], v173 offset:52224
	ds_read_b128 v[46:49], v173 offset:53248
	ds_read_b128 v[58:61], v173 offset:54272
	ds_read_b128 v[70:73], v173 offset:55296
	ds_read_b128 v[86:89], v173 offset:56320
	s_barrier
	s_waitcnt lgkmcnt(0)
	v_mfma_f32_16x16x32_f16 v[26:29], v[14:17], v[110:113], v[26:29]
	v_mfma_f32_16x16x32_f16 v[174:177], v[22:25], v[130:133], v[26:29]
	v_mfma_f32_16x16x32_f16 v[26:29], v[14:17], v[216:219], v[38:41]
	v_mfma_f32_16x16x32_f16 v[142:145], v[22:25], v[224:227], v[26:29]
	v_mfma_f32_16x16x32_f16 v[26:29], v[30:33], v[110:113], v[50:53]
	v_mfma_f32_16x16x32_f16 v[170:173], v[34:37], v[130:133], v[26:29]
	v_mfma_f32_16x16x32_f16 v[26:29], v[30:33], v[216:219], v[62:65]
	v_mfma_f32_16x16x32_f16 v[138:141], v[34:37], v[224:227], v[26:29]
	v_mfma_f32_16x16x32_f16 v[26:29], v[46:49], v[110:113], v[74:77]
	v_mfma_f32_16x16x32_f16 v[166:169], v[58:61], v[130:133], v[26:29]
	v_mfma_f32_16x16x32_f16 v[26:29], v[46:49], v[216:219], v[82:85]
	v_mfma_f32_16x16x32_f16 v[134:137], v[58:61], v[224:227], v[26:29]
	v_mfma_f32_16x16x32_f16 v[26:29], v[70:73], v[110:113], v[90:93]
	v_mfma_f32_16x16x32_f16 v[162:165], v[86:89], v[130:133], v[26:29]
	v_mfma_f32_16x16x32_f16 v[26:29], v[70:73], v[216:219], v[94:97]
	v_mfma_f32_16x16x32_f16 v[130:133], v[86:89], v[224:227], v[26:29]
	v_mfma_f32_16x16x32_f16 v[26:29], v[14:17], v[2:5], v[98:101]
	v_mfma_f32_16x16x32_f16 v[14:17], v[14:17], v[10:13], v[102:105]
	v_mfma_f32_16x16x32_f16 v[38:41], v[22:25], v[18:21], v[14:17]
	v_mfma_f32_16x16x32_f16 v[14:17], v[30:33], v[2:5], v[106:109]
	v_mfma_f32_16x16x32_f16 v[106:109], v[34:37], v[6:9], v[14:17]
	v_mfma_f32_16x16x32_f16 v[14:17], v[30:33], v[10:13], v[200:203]
	v_mfma_f32_16x16x32_f16 v[110:113], v[22:25], v[6:9], v[26:29]
	v_mfma_f32_16x16x32_f16 v[26:29], v[34:37], v[18:21], v[14:17]
	v_mfma_f32_16x16x32_f16 v[14:17], v[46:49], v[2:5], v[204:207]
	v_mfma_f32_16x16x32_f16 v[2:5], v[70:73], v[2:5], v[212:215]
	v_mfma_f32_16x16x32_f16 v[102:105], v[58:61], v[6:9], v[14:17]
	v_mfma_f32_16x16x32_f16 v[14:17], v[46:49], v[10:13], v[220:223]
	v_mfma_f32_16x16x32_f16 v[98:101], v[86:89], v[6:9], v[2:5]
	v_mfma_f32_16x16x32_f16 v[2:5], v[70:73], v[10:13], v[196:199]
	v_mfma_f32_16x16x32_f16 v[14:17], v[58:61], v[18:21], v[14:17]
	v_mfma_f32_16x16x32_f16 v[2:5], v[86:89], v[18:21], v[2:5]
	s_cmpk_gt_u32 s65, 0xff
	s_barrier
	s_cbranch_scc1 .LBB6_15
	s_barrier

.LBB7_239:
	ds_read_b128 v[176:179], v169
	ds_read_b128 v[180:183], v170
	ds_read_b128 v[184:187], v171
	ds_read_b128 v[188:191], v172
	v_add_u32_e32 v174, 0xc000, v152
	v_lshl_add_u64 v[192:193], v[136:137], 0, s[46:47]
	v_add_u32_e32 v175, 0xe000, v152
	v_add_u32_e32 v173, s5, v168
	ds_read_b128 v[196:199], v173
	ds_read_b128 v[200:203], v173 offset:1024
	ds_read_b128 v[204:207], v173 offset:2048
	ds_read_b128 v[212:215], v173 offset:3072
	ds_read_b128 v[216:219], v173 offset:4096
	ds_read_b128 v[220:223], v173 offset:5120
	ds_read_b128 v[224:227], v173 offset:6144
	ds_read_b128 v[228:231], v173 offset:7168
	v_lshl_add_u64 v[232:233], v[192:193], 0, s[34:35]
	s_mov_b32 m0, s72
	v_lshl_add_u64 v[248:249], v[134:135], 0, s[46:47]
	global_load_lds_dwordx4 v[232:233], off
	s_mov_b32 m0, s73
	v_lshl_add_u64 v[232:233], v[248:249], 0, s[34:35]
	global_load_lds_dwordx4 v[232:233], off
	s_waitcnt lgkmcnt(8)
	s_barrier
	s_waitcnt lgkmcnt(0)
	v_mfma_f32_16x16x32_f16 v[2:5], v[196:199], v[176:179], v[2:5]
	v_mfma_f32_16x16x32_f16 v[6:9], v[196:199], v[184:187], v[6:9]
	v_mfma_f32_16x16x32_f16 v[10:13], v[204:207], v[176:179], v[10:13]
	v_mfma_f32_16x16x32_f16 v[18:21], v[204:207], v[184:187], v[18:21]
	v_mfma_f32_16x16x32_f16 v[30:33], v[216:219], v[176:179], v[30:33]
	v_mfma_f32_16x16x32_f16 v[42:45], v[216:219], v[184:187], v[42:45]
	v_mfma_f32_16x16x32_f16 v[54:57], v[224:227], v[176:179], v[54:57]
	v_mfma_f32_16x16x32_f16 v[66:69], v[224:227], v[184:187], v[66:69]
	v_mfma_f32_16x16x32_f16 v[2:5], v[200:203], v[180:183], v[2:5]
	v_mfma_f32_16x16x32_f16 v[6:9], v[200:203], v[188:191], v[6:9]
	v_mfma_f32_16x16x32_f16 v[10:13], v[212:215], v[180:183], v[10:13]
	v_mfma_f32_16x16x32_f16 v[18:21], v[212:215], v[188:191], v[18:21]
	v_mfma_f32_16x16x32_f16 v[30:33], v[220:223], v[180:183], v[30:33]
	v_mfma_f32_16x16x32_f16 v[42:45], v[220:223], v[188:191], v[42:45]
	v_mfma_f32_16x16x32_f16 v[54:57], v[228:231], v[180:183], v[54:57]
	v_mfma_f32_16x16x32_f16 v[66:69], v[228:231], v[188:191], v[66:69]
	s_barrier
	v_lshl_add_u64 v[250:251], v[140:141], 0, s[46:47]
	v_lshl_add_u64 v[252:253], v[250:251], 0, s[36:37]
	s_mov_b32 m0, s74
	ds_read_b128 v[232:235], v161
	ds_read_b128 v[236:239], v162
	ds_read_b128 v[240:243], v163
	ds_read_b128 v[244:247], v164
	global_load_lds_dwordx4 v[252:253], off
	v_lshl_add_u64 v[252:253], v[138:139], 0, s[46:47]
	s_mov_b32 m0, s75
	v_lshl_add_u64 v[254:255], v[252:253], 0, s[36:37]
	global_load_lds_dwordx4 v[254:255], off
	s_barrier
	s_waitcnt lgkmcnt(0)
	v_mfma_f32_16x16x32_f16 v[14:17], v[196:199], v[232:235], v[14:17]
	v_mfma_f32_16x16x32_f16 v[22:25], v[196:199], v[240:243], v[22:25]
	v_mfma_f32_16x16x32_f16 v[34:37], v[204:207], v[232:235], v[34:37]
	v_mfma_f32_16x16x32_f16 v[46:49], v[204:207], v[240:243], v[46:49]
	v_mfma_f32_16x16x32_f16 v[58:61], v[216:219], v[232:235], v[58:61]
	v_mfma_f32_16x16x32_f16 v[70:73], v[216:219], v[240:243], v[70:73]
	v_mfma_f32_16x16x32_f16 v[78:81], v[224:227], v[232:235], v[78:81]
	v_mfma_f32_16x16x32_f16 v[86:89], v[224:227], v[240:243], v[86:89]
	v_mfma_f32_16x16x32_f16 v[14:17], v[200:203], v[236:239], v[14:17]
	v_mfma_f32_16x16x32_f16 v[22:25], v[200:203], v[244:247], v[22:25]
	v_mfma_f32_16x16x32_f16 v[34:37], v[212:215], v[236:239], v[34:37]
	v_mfma_f32_16x16x32_f16 v[46:49], v[212:215], v[244:247], v[46:49]
	v_mfma_f32_16x16x32_f16 v[58:61], v[220:223], v[236:239], v[58:61]
	v_mfma_f32_16x16x32_f16 v[70:73], v[220:223], v[244:247], v[70:73]
	v_mfma_f32_16x16x32_f16 v[78:81], v[228:231], v[236:239], v[78:81]
	v_mfma_f32_16x16x32_f16 v[86:89], v[228:231], v[244:247], v[86:89]
	v_lshl_add_u64 v[254:255], v[192:193], 0, s[36:37]
	s_mov_b32 m0, s76
	s_barrier
	ds_read_b128 v[196:199], v173 offset:16384
	ds_read_b128 v[200:203], v173 offset:17408
	ds_read_b128 v[204:207], v173 offset:18432
	ds_read_b128 v[212:215], v173 offset:19456
	ds_read_b128 v[216:219], v173 offset:20480
	ds_read_b128 v[220:223], v173 offset:21504
	ds_read_b128 v[224:227], v173 offset:22528
	ds_read_b128 v[228:231], v173 offset:23552
	global_load_lds_dwordx4 v[254:255], off
	s_mov_b32 m0, s77
	v_lshl_add_u64 v[254:255], v[248:249], 0, s[36:37]
	global_load_lds_dwordx4 v[254:255], off
	s_barrier
	s_waitcnt lgkmcnt(0)
	v_mfma_f32_16x16x32_f16 v[26:29], v[196:199], v[176:179], v[26:29]
	v_mfma_f32_16x16x32_f16 v[38:41], v[196:199], v[184:187], v[38:41]
	v_mfma_f32_16x16x32_f16 v[50:53], v[204:207], v[176:179], v[50:53]
	v_mfma_f32_16x16x32_f16 v[62:65], v[204:207], v[184:187], v[62:65]
	v_mfma_f32_16x16x32_f16 v[74:77], v[216:219], v[176:179], v[74:77]
	v_mfma_f32_16x16x32_f16 v[82:85], v[216:219], v[184:187], v[82:85]
	v_mfma_f32_16x16x32_f16 v[90:93], v[224:227], v[176:179], v[90:93]
	v_mfma_f32_16x16x32_f16 v[94:97], v[224:227], v[184:187], v[94:97]
	v_mfma_f32_16x16x32_f16 v[26:29], v[200:203], v[180:183], v[26:29]
	v_mfma_f32_16x16x32_f16 v[38:41], v[200:203], v[188:191], v[38:41]
	v_mfma_f32_16x16x32_f16 v[50:53], v[212:215], v[180:183], v[50:53]
	v_mfma_f32_16x16x32_f16 v[62:65], v[212:215], v[188:191], v[62:65]
	v_mfma_f32_16x16x32_f16 v[74:77], v[220:223], v[180:183], v[74:77]
	v_mfma_f32_16x16x32_f16 v[82:85], v[220:223], v[188:191], v[82:85]
	v_mfma_f32_16x16x32_f16 v[90:93], v[228:231], v[180:183], v[90:93]
	v_mfma_f32_16x16x32_f16 v[94:97], v[228:231], v[188:191], v[94:97]
	s_barrier
	s_mov_b32 m0, s78
	v_lshl_add_u64 v[176:177], v[250:251], 0, s[38:39]
	global_load_lds_dwordx4 v[176:177], off
	s_mov_b32 m0, s79
	v_lshl_add_u64 v[176:177], v[252:253], 0, s[38:39]
	global_load_lds_dwordx4 v[176:177], off
	s_waitcnt vmcnt(6)
	s_barrier
	v_mfma_f32_16x16x32_f16 v[98:101], v[196:199], v[232:235], v[98:101]
	v_mfma_f32_16x16x32_f16 v[102:105], v[196:199], v[240:243], v[102:105]
	v_mfma_f32_16x16x32_f16 v[106:109], v[204:207], v[232:235], v[106:109]
	v_mfma_f32_16x16x32_f16 v[110:113], v[204:207], v[240:243], v[110:113]
	v_mfma_f32_16x16x32_f16 v[114:117], v[216:219], v[232:235], v[114:117]
	v_mfma_f32_16x16x32_f16 v[118:121], v[216:219], v[240:243], v[118:121]
	v_mfma_f32_16x16x32_f16 v[122:125], v[224:227], v[232:235], v[122:125]
	v_mfma_f32_16x16x32_f16 v[126:129], v[224:227], v[240:243], v[126:129]
	v_mfma_f32_16x16x32_f16 v[98:101], v[200:203], v[236:239], v[98:101]
	v_mfma_f32_16x16x32_f16 v[102:105], v[200:203], v[244:247], v[102:105]
	v_mfma_f32_16x16x32_f16 v[106:109], v[212:215], v[236:239], v[106:109]
	v_mfma_f32_16x16x32_f16 v[110:113], v[212:215], v[244:247], v[110:113]
	v_mfma_f32_16x16x32_f16 v[114:117], v[220:223], v[236:239], v[114:117]
	v_mfma_f32_16x16x32_f16 v[118:121], v[220:223], v[244:247], v[118:121]
	v_mfma_f32_16x16x32_f16 v[122:125], v[228:231], v[236:239], v[122:125]
	v_mfma_f32_16x16x32_f16 v[126:129], v[228:231], v[244:247], v[126:129]
	s_barrier
	ds_read_b128 v[176:179], v148
	ds_read_b128 v[180:183], v149
	ds_read_b128 v[184:187], v150
	ds_read_b128 v[188:191], v151
	ds_read_b128 v[196:199], v173 offset:32768
	ds_read_b128 v[200:203], v173 offset:33792
	ds_read_b128 v[204:207], v173 offset:34816
	ds_read_b128 v[212:215], v173 offset:35840
	ds_read_b128 v[216:219], v173 offset:36864
	ds_read_b128 v[220:223], v173 offset:37888
	ds_read_b128 v[224:227], v173 offset:38912
	ds_read_b128 v[228:231], v173 offset:39936
	s_mov_b32 m0, s80
	v_lshl_add_u64 v[232:233], v[192:193], 0, s[38:39]
	global_load_lds_dwordx4 v[232:233], off
	s_mov_b32 m0, s81
	v_lshl_add_u64 v[232:233], v[248:249], 0, s[38:39]
	global_load_lds_dwordx4 v[232:233], off
	s_waitcnt lgkmcnt(8)
	s_barrier
	s_waitcnt lgkmcnt(0)
	v_mfma_f32_16x16x32_f16 v[2:5], v[196:199], v[176:179], v[2:5]
	v_mfma_f32_16x16x32_f16 v[6:9], v[196:199], v[184:187], v[6:9]
	v_mfma_f32_16x16x32_f16 v[10:13], v[204:207], v[176:179], v[10:13]
	v_mfma_f32_16x16x32_f16 v[18:21], v[204:207], v[184:187], v[18:21]
	v_mfma_f32_16x16x32_f16 v[30:33], v[216:219], v[176:179], v[30:33]
	v_mfma_f32_16x16x32_f16 v[42:45], v[216:219], v[184:187], v[42:45]
	v_mfma_f32_16x16x32_f16 v[54:57], v[224:227], v[176:179], v[54:57]
	v_mfma_f32_16x16x32_f16 v[66:69], v[224:227], v[184:187], v[66:69]
	v_mfma_f32_16x16x32_f16 v[2:5], v[200:203], v[180:183], v[2:5]
	v_mfma_f32_16x16x32_f16 v[6:9], v[200:203], v[188:191], v[6:9]
	v_mfma_f32_16x16x32_f16 v[10:13], v[212:215], v[180:183], v[10:13]
	v_mfma_f32_16x16x32_f16 v[18:21], v[212:215], v[188:191], v[18:21]
	v_mfma_f32_16x16x32_f16 v[30:33], v[220:223], v[180:183], v[30:33]
	v_mfma_f32_16x16x32_f16 v[42:45], v[220:223], v[188:191], v[42:45]
	v_mfma_f32_16x16x32_f16 v[54:57], v[228:231], v[180:183], v[54:57]
	v_mfma_f32_16x16x32_f16 v[66:69], v[228:231], v[188:191], v[66:69]
	s_barrier
	v_lshl_add_u64 v[254:255], v[250:251], 0, s[40:41]
	s_mov_b32 m0, s82
	ds_read_b128 v[232:235], v142
	ds_read_b128 v[236:239], v143
	ds_read_b128 v[240:243], v144
	ds_read_b128 v[244:247], v145
	global_load_lds_dwordx4 v[254:255], off
	s_mov_b32 m0, s83
	v_lshl_add_u64 v[254:255], v[252:253], 0, s[40:41]
	global_load_lds_dwordx4 v[254:255], off
	s_barrier
	s_waitcnt lgkmcnt(0)
	v_mfma_f32_16x16x32_f16 v[14:17], v[196:199], v[232:235], v[14:17]
	v_mfma_f32_16x16x32_f16 v[22:25], v[196:199], v[240:243], v[22:25]
	v_mfma_f32_16x16x32_f16 v[34:37], v[204:207], v[232:235], v[34:37]
	v_mfma_f32_16x16x32_f16 v[46:49], v[204:207], v[240:243], v[46:49]
	v_mfma_f32_16x16x32_f16 v[58:61], v[216:219], v[232:235], v[58:61]
	v_mfma_f32_16x16x32_f16 v[70:73], v[216:219], v[240:243], v[70:73]
	v_mfma_f32_16x16x32_f16 v[78:81], v[224:227], v[232:235], v[78:81]
	v_mfma_f32_16x16x32_f16 v[86:89], v[224:227], v[240:243], v[86:89]
	v_mfma_f32_16x16x32_f16 v[14:17], v[200:203], v[236:239], v[14:17]
	v_mfma_f32_16x16x32_f16 v[22:25], v[200:203], v[244:247], v[22:25]
	v_mfma_f32_16x16x32_f16 v[34:37], v[212:215], v[236:239], v[34:37]
	v_mfma_f32_16x16x32_f16 v[46:49], v[212:215], v[244:247], v[46:49]
	v_mfma_f32_16x16x32_f16 v[58:61], v[220:223], v[236:239], v[58:61]
	v_mfma_f32_16x16x32_f16 v[70:73], v[220:223], v[244:247], v[70:73]
	v_mfma_f32_16x16x32_f16 v[78:81], v[228:231], v[236:239], v[78:81]
	v_mfma_f32_16x16x32_f16 v[86:89], v[228:231], v[244:247], v[86:89]
	v_lshl_add_u64 v[192:193], v[192:193], 0, s[40:41]
	s_mov_b32 m0, s84
	s_barrier
	ds_read_b128 v[196:199], v173 offset:49152
	ds_read_b128 v[200:203], v173 offset:50176
	ds_read_b128 v[204:207], v173 offset:51200
	ds_read_b128 v[212:215], v173 offset:52224
	ds_read_b128 v[216:219], v173 offset:53248
	ds_read_b128 v[220:223], v173 offset:54272
	ds_read_b128 v[224:227], v173 offset:55296
	ds_read_b128 v[228:231], v173 offset:56320
	global_load_lds_dwordx4 v[192:193], off
	s_mov_b32 m0, s85
	v_lshl_add_u64 v[192:193], v[248:249], 0, s[40:41]
	global_load_lds_dwordx4 v[192:193], off
	s_barrier
	s_waitcnt lgkmcnt(0)
	v_mfma_f32_16x16x32_f16 v[26:29], v[196:199], v[176:179], v[26:29]
	v_mfma_f32_16x16x32_f16 v[38:41], v[196:199], v[184:187], v[38:41]
	v_mfma_f32_16x16x32_f16 v[50:53], v[204:207], v[176:179], v[50:53]
	v_mfma_f32_16x16x32_f16 v[62:65], v[204:207], v[184:187], v[62:65]
	v_mfma_f32_16x16x32_f16 v[74:77], v[216:219], v[176:179], v[74:77]
	v_mfma_f32_16x16x32_f16 v[82:85], v[216:219], v[184:187], v[82:85]
	v_mfma_f32_16x16x32_f16 v[90:93], v[224:227], v[176:179], v[90:93]
	v_mfma_f32_16x16x32_f16 v[94:97], v[224:227], v[184:187], v[94:97]
	v_mfma_f32_16x16x32_f16 v[26:29], v[200:203], v[180:183], v[26:29]
	v_mfma_f32_16x16x32_f16 v[38:41], v[200:203], v[188:191], v[38:41]
	v_mfma_f32_16x16x32_f16 v[50:53], v[212:215], v[180:183], v[50:53]
	v_mfma_f32_16x16x32_f16 v[62:65], v[212:215], v[188:191], v[62:65]
	v_mfma_f32_16x16x32_f16 v[74:77], v[220:223], v[180:183], v[74:77]
	v_mfma_f32_16x16x32_f16 v[82:85], v[220:223], v[188:191], v[82:85]
	v_mfma_f32_16x16x32_f16 v[90:93], v[228:231], v[180:183], v[90:93]
	v_mfma_f32_16x16x32_f16 v[94:97], v[228:231], v[188:191], v[94:97]
	s_barrier
	s_mov_b32 m0, s86
	v_lshl_add_u64 v[176:177], v[250:251], 0, s[42:43]
	global_load_lds_dwordx4 v[176:177], off
	s_mov_b32 m0, s87
	v_lshl_add_u64 v[176:177], v[252:253], 0, s[42:43]
	global_load_lds_dwordx4 v[176:177], off
	s_waitcnt vmcnt(6)
	s_barrier
	v_mfma_f32_16x16x32_f16 v[98:101], v[196:199], v[232:235], v[98:101]
	v_mfma_f32_16x16x32_f16 v[102:105], v[196:199], v[240:243], v[102:105]
	v_mfma_f32_16x16x32_f16 v[106:109], v[204:207], v[232:235], v[106:109]
	v_mfma_f32_16x16x32_f16 v[110:113], v[204:207], v[240:243], v[110:113]
	v_mfma_f32_16x16x32_f16 v[114:117], v[216:219], v[232:235], v[114:117]
	v_mfma_f32_16x16x32_f16 v[118:121], v[216:219], v[240:243], v[118:121]
	v_mfma_f32_16x16x32_f16 v[122:125], v[224:227], v[232:235], v[122:125]
	v_mfma_f32_16x16x32_f16 v[126:129], v[224:227], v[240:243], v[126:129]
	v_mfma_f32_16x16x32_f16 v[98:101], v[200:203], v[236:239], v[98:101]
	v_mfma_f32_16x16x32_f16 v[102:105], v[200:203], v[244:247], v[102:105]
	v_mfma_f32_16x16x32_f16 v[106:109], v[212:215], v[236:239], v[106:109]
	v_mfma_f32_16x16x32_f16 v[110:113], v[212:215], v[244:247], v[110:113]
	v_mfma_f32_16x16x32_f16 v[114:117], v[220:223], v[236:239], v[114:117]
	v_mfma_f32_16x16x32_f16 v[118:121], v[220:223], v[244:247], v[118:121]
	v_mfma_f32_16x16x32_f16 v[122:125], v[228:231], v[236:239], v[122:125]
	v_mfma_f32_16x16x32_f16 v[126:129], v[228:231], v[244:247], v[126:129]
	s_add_i32 s48, s48, 2
	s_add_u32 s46, s46, 0x100
	s_addc_u32 s47, s47, 0
	s_cmp_lt_u32 s48, 4
	s_barrier
	s_cbranch_scc1 .LBB7_239
	s_add_u32 s0, s0, 0x20380
	s_addc_u32 s1, s1, 0
	v_readfirstlane_b32 s5, v174
	v_lshl_add_u64 v[130:131], v[130:131], 1, s[0:1]
	s_mov_b32 m0, s5
	ds_read_b128 v[134:137], v169
	ds_read_b128 v[138:141], v170
	ds_read_b128 v[152:155], v171
	ds_read_b128 v[156:159], v172
	ds_read_b128 v[166:169], v173
	ds_read_b128 v[176:179], v173 offset:1024
	ds_read_b128 v[180:183], v173 offset:2048
	ds_read_b128 v[184:187], v173 offset:3072
	ds_read_b128 v[188:191], v173 offset:4096
	ds_read_b128 v[196:199], v173 offset:5120
	ds_read_b128 v[200:203], v173 offset:6144
	ds_read_b128 v[204:207], v173 offset:7168
	global_load_lds_dwordx4 v[130:131], off
	v_lshl_add_u64 v[130:131], v[132:133], 1, s[0:1]
	v_readfirstlane_b32 s0, v175
	s_mov_b32 m0, s0
	s_nop 0
	global_load_lds_dwordx4 v[130:131], off
	s_barrier
	s_waitcnt lgkmcnt(0)
	v_mfma_f32_16x16x32_f16 v[2:5], v[166:169], v[134:137], v[2:5]
	v_mfma_f32_16x16x32_f16 v[42:45], v[188:191], v[152:155], v[42:45]
	v_mfma_f32_16x16x32_f16 v[54:57], v[200:203], v[134:137], v[54:57]
	v_mfma_f32_16x16x32_f16 v[66:69], v[200:203], v[152:155], v[66:69]
	v_mfma_f32_16x16x32_f16 v[2:5], v[176:179], v[138:141], v[2:5]
	v_mfma_f32_16x16x32_f16 v[6:9], v[166:169], v[152:155], v[6:9]
	v_mfma_f32_16x16x32_f16 v[10:13], v[180:183], v[134:137], v[10:13]
	v_mfma_f32_16x16x32_f16 v[18:21], v[180:183], v[152:155], v[18:21]
	v_mfma_f32_16x16x32_f16 v[30:33], v[188:191], v[134:137], v[30:33]
	v_mfma_f32_16x16x32_f16 v[42:45], v[196:199], v[156:159], v[42:45]
	v_mfma_f32_16x16x32_f16 v[54:57], v[204:207], v[138:141], v[54:57]
	v_mfma_f32_16x16x32_f16 v[66:69], v[204:207], v[156:159], v[66:69]
	v_mfma_f32_16x16x32_f16 v[6:9], v[176:179], v[156:159], v[6:9]
	v_mfma_f32_16x16x32_f16 v[10:13], v[184:187], v[138:141], v[10:13]
	v_mfma_f32_16x16x32_f16 v[18:21], v[184:187], v[156:159], v[18:21]
	v_mfma_f32_16x16x32_f16 v[30:33], v[196:199], v[138:141], v[30:33]
	s_barrier
	ds_read_b128 v[130:133], v161
	ds_read_b128 v[212:215], v162
	ds_read_b128 v[160:163], v163
	ds_read_b128 v[216:219], v164
	s_barrier
	s_waitcnt lgkmcnt(0)
	v_mfma_f32_16x16x32_f16 v[14:17], v[166:169], v[130:133], v[14:17]
	v_mfma_f32_16x16x32_f16 v[78:81], v[200:203], v[130:133], v[78:81]
	v_mfma_f32_16x16x32_f16 v[14:17], v[176:179], v[212:215], v[14:17]
	v_mfma_f32_16x16x32_f16 v[22:25], v[166:169], v[160:163], v[22:25]
	v_mfma_f32_16x16x32_f16 v[34:37], v[180:183], v[130:133], v[34:37]
	v_mfma_f32_16x16x32_f16 v[46:49], v[180:183], v[160:163], v[46:49]
	v_mfma_f32_16x16x32_f16 v[58:61], v[188:191], v[130:133], v[58:61]
	v_mfma_f32_16x16x32_f16 v[70:73], v[188:191], v[160:163], v[70:73]
	v_mfma_f32_16x16x32_f16 v[164:167], v[204:207], v[212:215], v[78:81]
	v_mfma_f32_16x16x32_f16 v[78:81], v[200:203], v[160:163], v[86:89]
	v_mfma_f32_16x16x32_f16 v[22:25], v[176:179], v[216:219], v[22:25]
	v_mfma_f32_16x16x32_f16 v[34:37], v[184:187], v[212:215], v[34:37]
	v_mfma_f32_16x16x32_f16 v[46:49], v[184:187], v[216:219], v[46:49]
	v_mfma_f32_16x16x32_f16 v[58:61], v[196:199], v[212:215], v[58:61]
	v_mfma_f32_16x16x32_f16 v[70:73], v[196:199], v[216:219], v[70:73]
	v_mfma_f32_16x16x32_f16 v[86:89], v[204:207], v[216:219], v[78:81]
	s_barrier
	s_nop 0
	ds_read_b128 v[78:81], v173 offset:16384
	ds_read_b128 v[168:171], v173 offset:17408
	ds_read_b128 v[174:177], v173 offset:18432
	ds_read_b128 v[178:181], v173 offset:19456
	ds_read_b128 v[182:185], v173 offset:20480
	ds_read_b128 v[186:189], v173 offset:21504
	ds_read_b128 v[190:193], v173 offset:22528
	ds_read_b128 v[196:199], v173 offset:23552
	s_waitcnt vmcnt(4)
	s_barrier
	s_waitcnt lgkmcnt(0)
	v_mfma_f32_16x16x32_f16 v[26:29], v[78:81], v[134:137], v[26:29]
	v_mfma_f32_16x16x32_f16 v[38:41], v[78:81], v[152:155], v[38:41]
	v_mfma_f32_16x16x32_f16 v[26:29], v[168:171], v[138:141], v[26:29]
	v_mfma_f32_16x16x32_f16 v[38:41], v[168:171], v[156:159], v[38:41]
	v_mfma_f32_16x16x32_f16 v[50:53], v[174:177], v[134:137], v[50:53]
	v_mfma_f32_16x16x32_f16 v[62:65], v[174:177], v[152:155], v[62:65]
	v_mfma_f32_16x16x32_f16 v[74:77], v[182:185], v[134:137], v[74:77]
	v_mfma_f32_16x16x32_f16 v[82:85], v[182:185], v[152:155], v[82:85]
	v_mfma_f32_16x16x32_f16 v[90:93], v[190:193], v[134:137], v[90:93]
	v_mfma_f32_16x16x32_f16 v[94:97], v[190:193], v[152:155], v[94:97]
	v_mfma_f32_16x16x32_f16 v[50:53], v[178:181], v[138:141], v[50:53]
	v_mfma_f32_16x16x32_f16 v[62:65], v[178:181], v[156:159], v[62:65]
	v_mfma_f32_16x16x32_f16 v[74:77], v[186:189], v[138:141], v[74:77]
	v_mfma_f32_16x16x32_f16 v[82:85], v[186:189], v[156:159], v[82:85]
	v_mfma_f32_16x16x32_f16 v[90:93], v[196:199], v[138:141], v[90:93]
	v_mfma_f32_16x16x32_f16 v[94:97], v[196:199], v[156:159], v[94:97]
	v_mfma_f32_16x16x32_f16 v[98:101], v[78:81], v[130:133], v[98:101]
	v_mfma_f32_16x16x32_f16 v[78:81], v[78:81], v[160:163], v[102:105]
	v_mfma_f32_16x16x32_f16 v[102:105], v[168:171], v[216:219], v[78:81]
	v_mfma_f32_16x16x32_f16 v[78:81], v[174:177], v[130:133], v[106:109]
	v_mfma_f32_16x16x32_f16 v[106:109], v[178:181], v[212:215], v[78:81]
	v_mfma_f32_16x16x32_f16 v[78:81], v[174:177], v[160:163], v[110:113]
	v_mfma_f32_16x16x32_f16 v[200:203], v[178:181], v[216:219], v[78:81]
	v_mfma_f32_16x16x32_f16 v[78:81], v[182:185], v[130:133], v[114:117]
	v_mfma_f32_16x16x32_f16 v[204:207], v[186:189], v[212:215], v[78:81]
	v_mfma_f32_16x16x32_f16 v[78:81], v[182:185], v[160:163], v[118:121]
	v_mfma_f32_16x16x32_f16 v[220:223], v[186:189], v[216:219], v[78:81]
	v_mfma_f32_16x16x32_f16 v[78:81], v[190:193], v[130:133], v[122:125]
	v_mfma_f32_16x16x32_f16 v[98:101], v[168:171], v[212:215], v[98:101]
	v_mfma_f32_16x16x32_f16 v[212:215], v[196:199], v[212:215], v[78:81]
	v_mfma_f32_16x16x32_f16 v[78:81], v[190:193], v[160:163], v[126:129]
	v_mfma_f32_16x16x32_f16 v[196:199], v[196:199], v[216:219], v[78:81]
	s_barrier
	ds_read_b128 v[110:113], v148
	ds_read_b128 v[130:133], v149
	ds_read_b128 v[216:219], v150
	ds_read_b128 v[224:227], v151
	s_nop 0
	ds_read_b128 v[78:81], v173 offset:32768
	ds_read_b128 v[114:117], v173 offset:33792
	ds_read_b128 v[118:121], v173 offset:34816
	ds_read_b128 v[134:137], v173 offset:35840
	ds_read_b128 v[138:141], v173 offset:36864
	ds_read_b128 v[168:171], v173 offset:37888
	ds_read_b128 v[174:177], v173 offset:38912
	ds_read_b128 v[228:231], v173 offset:39936
	s_waitcnt vmcnt(2)
	s_barrier
	s_waitcnt lgkmcnt(0)
	v_mfma_f32_16x16x32_f16 v[2:5], v[78:81], v[110:113], v[2:5]
	v_mfma_f32_16x16x32_f16 v[190:193], v[114:117], v[130:133], v[2:5]
	v_mfma_f32_16x16x32_f16 v[2:5], v[78:81], v[216:219], v[6:9]
	v_mfma_f32_16x16x32_f16 v[158:161], v[114:117], v[224:227], v[2:5]
	v_mfma_f32_16x16x32_f16 v[2:5], v[118:121], v[110:113], v[10:13]
	v_mfma_f32_16x16x32_f16 v[186:189], v[134:137], v[130:133], v[2:5]
	v_mfma_f32_16x16x32_f16 v[2:5], v[118:121], v[216:219], v[18:21]
	v_mfma_f32_16x16x32_f16 v[154:157], v[134:137], v[224:227], v[2:5]
	v_mfma_f32_16x16x32_f16 v[2:5], v[138:141], v[110:113], v[30:33]
	v_mfma_f32_16x16x32_f16 v[182:185], v[168:171], v[130:133], v[2:5]
	v_mfma_f32_16x16x32_f16 v[2:5], v[138:141], v[216:219], v[42:45]
	v_mfma_f32_16x16x32_f16 v[150:153], v[168:171], v[224:227], v[2:5]
	v_mfma_f32_16x16x32_f16 v[2:5], v[174:177], v[110:113], v[54:57]
	v_mfma_f32_16x16x32_f16 v[178:181], v[228:231], v[130:133], v[2:5]
	v_mfma_f32_16x16x32_f16 v[2:5], v[174:177], v[216:219], v[66:69]
	v_mfma_f32_16x16x32_f16 v[146:149], v[228:231], v[224:227], v[2:5]
	s_barrier
	s_nop 4
	ds_read_b128 v[2:5], v142
	ds_read_b128 v[6:9], v143
	ds_read_b128 v[10:13], v144
	ds_read_b128 v[18:21], v145
	s_waitcnt vmcnt(0)
	s_barrier
	s_waitcnt lgkmcnt(0)
	v_mfma_f32_16x16x32_f16 v[14:17], v[78:81], v[2:5], v[14:17]
	v_mfma_f32_16x16x32_f16 v[126:129], v[114:117], v[6:9], v[14:17]
	v_mfma_f32_16x16x32_f16 v[14:17], v[78:81], v[10:13], v[22:25]
	v_mfma_f32_16x16x32_f16 v[78:81], v[114:117], v[18:21], v[14:17]
	v_mfma_f32_16x16x32_f16 v[14:17], v[118:121], v[2:5], v[34:37]
	v_mfma_f32_16x16x32_f16 v[122:125], v[134:137], v[6:9], v[14:17]
	v_mfma_f32_16x16x32_f16 v[14:17], v[118:121], v[10:13], v[46:49]
	v_mfma_f32_16x16x32_f16 v[66:69], v[134:137], v[18:21], v[14:17]
	v_mfma_f32_16x16x32_f16 v[14:17], v[138:141], v[2:5], v[58:61]
	v_mfma_f32_16x16x32_f16 v[118:121], v[168:171], v[6:9], v[14:17]
	v_mfma_f32_16x16x32_f16 v[14:17], v[138:141], v[10:13], v[70:73]
	v_mfma_f32_16x16x32_f16 v[54:57], v[168:171], v[18:21], v[14:17]
	v_mfma_f32_16x16x32_f16 v[14:17], v[174:177], v[2:5], v[164:167]
	v_mfma_f32_16x16x32_f16 v[114:117], v[228:231], v[6:9], v[14:17]
	v_mfma_f32_16x16x32_f16 v[14:17], v[174:177], v[10:13], v[86:89]
	v_mfma_f32_16x16x32_f16 v[42:45], v[228:231], v[18:21], v[14:17]
	s_barrier
	s_nop 4
	ds_read_b128 v[14:17], v173 offset:49152
	ds_read_b128 v[22:25], v173 offset:50176
	ds_read_b128 v[30:33], v173 offset:51200
	ds_read_b128 v[34:37], v173 offset:52224
	ds_read_b128 v[46:49], v173 offset:53248
	ds_read_b128 v[58:61], v173 offset:54272
	ds_read_b128 v[70:73], v173 offset:55296
	ds_read_b128 v[86:89], v173 offset:56320
	s_barrier
	s_waitcnt lgkmcnt(0)
	v_mfma_f32_16x16x32_f16 v[26:29], v[14:17], v[110:113], v[26:29]
	v_mfma_f32_16x16x32_f16 v[174:177], v[22:25], v[130:133], v[26:29]
	v_mfma_f32_16x16x32_f16 v[26:29], v[14:17], v[216:219], v[38:41]
	v_mfma_f32_16x16x32_f16 v[142:145], v[22:25], v[224:227], v[26:29]
	v_mfma_f32_16x16x32_f16 v[26:29], v[30:33], v[110:113], v[50:53]
	v_mfma_f32_16x16x32_f16 v[170:173], v[34:37], v[130:133], v[26:29]
	v_mfma_f32_16x16x32_f16 v[26:29], v[30:33], v[216:219], v[62:65]
	v_mfma_f32_16x16x32_f16 v[138:141], v[34:37], v[224:227], v[26:29]
	v_mfma_f32_16x16x32_f16 v[26:29], v[46:49], v[110:113], v[74:77]
	v_mfma_f32_16x16x32_f16 v[166:169], v[58:61], v[130:133], v[26:29]
	v_mfma_f32_16x16x32_f16 v[26:29], v[46:49], v[216:219], v[82:85]
	v_mfma_f32_16x16x32_f16 v[134:137], v[58:61], v[224:227], v[26:29]
	v_mfma_f32_16x16x32_f16 v[26:29], v[70:73], v[110:113], v[90:93]
	v_mfma_f32_16x16x32_f16 v[162:165], v[86:89], v[130:133], v[26:29]
	v_mfma_f32_16x16x32_f16 v[26:29], v[70:73], v[216:219], v[94:97]
	v_mfma_f32_16x16x32_f16 v[130:133], v[86:89], v[224:227], v[26:29]
	v_mfma_f32_16x16x32_f16 v[26:29], v[14:17], v[2:5], v[98:101]
	v_mfma_f32_16x16x32_f16 v[14:17], v[14:17], v[10:13], v[102:105]
	v_mfma_f32_16x16x32_f16 v[38:41], v[22:25], v[18:21], v[14:17]
	v_mfma_f32_16x16x32_f16 v[14:17], v[30:33], v[2:5], v[106:109]
	v_mfma_f32_16x16x32_f16 v[106:109], v[34:37], v[6:9], v[14:17]
	v_mfma_f32_16x16x32_f16 v[14:17], v[30:33], v[10:13], v[200:203]
	v_mfma_f32_16x16x32_f16 v[110:113], v[22:25], v[6:9], v[26:29]
	v_mfma_f32_16x16x32_f16 v[26:29], v[34:37], v[18:21], v[14:17]
	v_mfma_f32_16x16x32_f16 v[14:17], v[46:49], v[2:5], v[204:207]
	v_mfma_f32_16x16x32_f16 v[2:5], v[70:73], v[2:5], v[212:215]
	v_mfma_f32_16x16x32_f16 v[102:105], v[58:61], v[6:9], v[14:17]
	v_mfma_f32_16x16x32_f16 v[14:17], v[46:49], v[10:13], v[220:223]
	v_mfma_f32_16x16x32_f16 v[98:101], v[86:89], v[6:9], v[2:5]
	v_mfma_f32_16x16x32_f16 v[2:5], v[70:73], v[10:13], v[196:199]
	v_mfma_f32_16x16x32_f16 v[14:17], v[58:61], v[18:21], v[14:17]
	v_mfma_f32_16x16x32_f16 v[2:5], v[86:89], v[18:21], v[2:5]
	s_cmpk_gt_u32 s65, 0xff
	s_barrier
	s_cbranch_scc1 .LBB7_242
	s_barrier

.LBB8_41:
	ds_read_b128 v[182:185], v171
	ds_read_b128 v[186:189], v173
	ds_read_b128 v[190:193], v174
	ds_read_b128 v[194:197], v175
	v_add_u32_e32 v177, 0xc000, v148
	v_lshl_add_u64 v[246:247], v[134:135], 0, s[44:45]
	v_add_u32_e32 v176, s48, v170
	ds_read_b128 v[198:201], v176
	ds_read_b128 v[202:205], v176 offset:1024
	ds_read_b128 v[206:209], v176 offset:2048
	ds_read_b128 v[210:213], v176 offset:3072
	ds_read_b128 v[214:217], v176 offset:4096
	ds_read_b128 v[218:221], v176 offset:5120
	ds_read_b128 v[222:225], v176 offset:6144
	ds_read_b128 v[226:229], v176 offset:7168
	s_mov_b32 m0, s75
	v_lshl_add_u64 v[178:179], v[246:247], 0, s[28:29]
	global_load_lds_dwordx4 v[178:179], off
	v_add_u32_e32 v178, 0xe000, v148
	v_lshl_add_u64 v[248:249], v[136:137], 0, s[44:45]
	s_mov_b32 m0, s76
	v_lshl_add_u64 v[230:231], v[248:249], 0, s[28:29]
	global_load_lds_dwordx4 v[230:231], off
	s_waitcnt lgkmcnt(8)
	s_barrier
	s_waitcnt lgkmcnt(0)
	v_mfma_f32_16x16x32_f16 v[126:129], v[198:201], v[182:185], v[126:129]
	v_mfma_f32_16x16x32_f16 v[122:125], v[198:201], v[190:193], v[122:125]
	v_mfma_f32_16x16x32_f16 v[118:121], v[206:209], v[182:185], v[118:121]
	v_mfma_f32_16x16x32_f16 v[114:117], v[206:209], v[190:193], v[114:117]
	v_mfma_f32_16x16x32_f16 v[110:113], v[214:217], v[182:185], v[110:113]
	v_mfma_f32_16x16x32_f16 v[106:109], v[214:217], v[190:193], v[106:109]
	v_mfma_f32_16x16x32_f16 v[102:105], v[222:225], v[182:185], v[102:105]
	v_mfma_f32_16x16x32_f16 v[98:101], v[222:225], v[190:193], v[98:101]
	v_mfma_f32_16x16x32_f16 v[126:129], v[202:205], v[186:189], v[126:129]
	v_mfma_f32_16x16x32_f16 v[122:125], v[202:205], v[194:197], v[122:125]
	v_mfma_f32_16x16x32_f16 v[118:121], v[210:213], v[186:189], v[118:121]
	v_mfma_f32_16x16x32_f16 v[114:117], v[210:213], v[194:197], v[114:117]
	v_mfma_f32_16x16x32_f16 v[110:113], v[218:221], v[186:189], v[110:113]
	v_mfma_f32_16x16x32_f16 v[106:109], v[218:221], v[194:197], v[106:109]
	v_mfma_f32_16x16x32_f16 v[102:105], v[226:229], v[186:189], v[102:105]
	v_mfma_f32_16x16x32_f16 v[98:101], v[226:229], v[194:197], v[98:101]
	s_barrier
	v_lshl_add_u64 v[250:251], v[138:139], 0, s[44:45]
	v_lshl_add_u64 v[252:253], v[250:251], 0, s[30:31]
	s_mov_b32 m0, s77
	ds_read_b128 v[230:233], v162
	ds_read_b128 v[234:237], v163
	ds_read_b128 v[238:241], v164
	ds_read_b128 v[242:245], v165
	global_load_lds_dwordx4 v[252:253], off
	v_lshl_add_u64 v[252:253], v[140:141], 0, s[44:45]
	s_mov_b32 m0, s78
	v_lshl_add_u64 v[254:255], v[252:253], 0, s[30:31]
	global_load_lds_dwordx4 v[254:255], off
	s_barrier
	s_waitcnt lgkmcnt(0)
	v_mfma_f32_16x16x32_f16 v[94:97], v[198:201], v[230:233], v[94:97]
	v_mfma_f32_16x16x32_f16 v[90:93], v[198:201], v[238:241], v[90:93]
	v_mfma_f32_16x16x32_f16 v[86:89], v[206:209], v[230:233], v[86:89]
	v_mfma_f32_16x16x32_f16 v[82:85], v[206:209], v[238:241], v[82:85]
	v_mfma_f32_16x16x32_f16 v[78:81], v[214:217], v[230:233], v[78:81]
	v_mfma_f32_16x16x32_f16 v[74:77], v[214:217], v[238:241], v[74:77]
	v_mfma_f32_16x16x32_f16 v[70:73], v[222:225], v[230:233], v[70:73]
	v_mfma_f32_16x16x32_f16 v[66:69], v[222:225], v[238:241], v[66:69]
	v_mfma_f32_16x16x32_f16 v[94:97], v[202:205], v[234:237], v[94:97]
	v_mfma_f32_16x16x32_f16 v[90:93], v[202:205], v[242:245], v[90:93]
	v_mfma_f32_16x16x32_f16 v[86:89], v[210:213], v[234:237], v[86:89]
	v_mfma_f32_16x16x32_f16 v[82:85], v[210:213], v[242:245], v[82:85]
	v_mfma_f32_16x16x32_f16 v[78:81], v[218:221], v[234:237], v[78:81]
	v_mfma_f32_16x16x32_f16 v[74:77], v[218:221], v[242:245], v[74:77]
	v_mfma_f32_16x16x32_f16 v[70:73], v[226:229], v[234:237], v[70:73]
	v_mfma_f32_16x16x32_f16 v[66:69], v[226:229], v[242:245], v[66:69]
	v_lshl_add_u64 v[254:255], v[246:247], 0, s[30:31]
	s_mov_b32 m0, s79
	s_barrier
	ds_read_b128 v[198:201], v176 offset:16384
	ds_read_b128 v[202:205], v176 offset:17408
	ds_read_b128 v[206:209], v176 offset:18432
	ds_read_b128 v[210:213], v176 offset:19456
	ds_read_b128 v[214:217], v176 offset:20480
	ds_read_b128 v[218:221], v176 offset:21504
	ds_read_b128 v[222:225], v176 offset:22528
	ds_read_b128 v[226:229], v176 offset:23552
	global_load_lds_dwordx4 v[254:255], off
	s_mov_b32 m0, s80
	v_lshl_add_u64 v[254:255], v[248:249], 0, s[30:31]
	global_load_lds_dwordx4 v[254:255], off
	s_barrier
	s_waitcnt lgkmcnt(0)
	v_mfma_f32_16x16x32_f16 v[62:65], v[198:201], v[182:185], v[62:65]
	v_mfma_f32_16x16x32_f16 v[58:61], v[198:201], v[190:193], v[58:61]
	v_mfma_f32_16x16x32_f16 v[54:57], v[206:209], v[182:185], v[54:57]
	v_mfma_f32_16x16x32_f16 v[50:53], v[206:209], v[190:193], v[50:53]
	v_mfma_f32_16x16x32_f16 v[46:49], v[214:217], v[182:185], v[46:49]
	v_mfma_f32_16x16x32_f16 v[42:45], v[214:217], v[190:193], v[42:45]
	v_mfma_f32_16x16x32_f16 v[38:41], v[222:225], v[182:185], v[38:41]
	v_mfma_f32_16x16x32_f16 v[34:37], v[222:225], v[190:193], v[34:37]
	v_mfma_f32_16x16x32_f16 v[62:65], v[202:205], v[186:189], v[62:65]
	v_mfma_f32_16x16x32_f16 v[58:61], v[202:205], v[194:197], v[58:61]
	v_mfma_f32_16x16x32_f16 v[54:57], v[210:213], v[186:189], v[54:57]
	v_mfma_f32_16x16x32_f16 v[50:53], v[210:213], v[194:197], v[50:53]
	v_mfma_f32_16x16x32_f16 v[46:49], v[218:221], v[186:189], v[46:49]
	v_mfma_f32_16x16x32_f16 v[42:45], v[218:221], v[194:197], v[42:45]
	v_mfma_f32_16x16x32_f16 v[38:41], v[226:229], v[186:189], v[38:41]
	v_mfma_f32_16x16x32_f16 v[34:37], v[226:229], v[194:197], v[34:37]
	s_barrier
	s_mov_b32 m0, s81
	v_lshl_add_u64 v[182:183], v[250:251], 0, s[34:35]
	global_load_lds_dwordx4 v[182:183], off
	s_mov_b32 m0, s82
	v_lshl_add_u64 v[182:183], v[252:253], 0, s[34:35]
	global_load_lds_dwordx4 v[182:183], off
	s_waitcnt vmcnt(6)
	s_barrier
	v_mfma_f32_16x16x32_f16 v[30:33], v[198:201], v[230:233], v[30:33]
	v_mfma_f32_16x16x32_f16 v[26:29], v[198:201], v[238:241], v[26:29]
	v_mfma_f32_16x16x32_f16 v[22:25], v[206:209], v[230:233], v[22:25]
	v_mfma_f32_16x16x32_f16 v[18:21], v[206:209], v[238:241], v[18:21]
	v_mfma_f32_16x16x32_f16 v[14:17], v[214:217], v[230:233], v[14:17]
	v_mfma_f32_16x16x32_f16 v[10:13], v[214:217], v[238:241], v[10:13]
	v_mfma_f32_16x16x32_f16 v[6:9], v[222:225], v[230:233], v[6:9]
	v_mfma_f32_16x16x32_f16 v[2:5], v[222:225], v[238:241], v[2:5]
	v_mfma_f32_16x16x32_f16 v[30:33], v[202:205], v[234:237], v[30:33]
	v_mfma_f32_16x16x32_f16 v[26:29], v[202:205], v[242:245], v[26:29]
	v_mfma_f32_16x16x32_f16 v[22:25], v[210:213], v[234:237], v[22:25]
	v_mfma_f32_16x16x32_f16 v[18:21], v[210:213], v[242:245], v[18:21]
	v_mfma_f32_16x16x32_f16 v[14:17], v[218:221], v[234:237], v[14:17]
	v_mfma_f32_16x16x32_f16 v[10:13], v[218:221], v[242:245], v[10:13]
	v_mfma_f32_16x16x32_f16 v[6:9], v[226:229], v[234:237], v[6:9]
	v_mfma_f32_16x16x32_f16 v[2:5], v[226:229], v[242:245], v[2:5]
	s_barrier
	ds_read_b128 v[182:185], v144
	ds_read_b128 v[186:189], v145
	ds_read_b128 v[190:193], v146
	ds_read_b128 v[194:197], v147
	ds_read_b128 v[198:201], v176 offset:32768
	ds_read_b128 v[202:205], v176 offset:33792
	ds_read_b128 v[206:209], v176 offset:34816
	ds_read_b128 v[210:213], v176 offset:35840
	ds_read_b128 v[214:217], v176 offset:36864
	ds_read_b128 v[218:221], v176 offset:37888
	ds_read_b128 v[222:225], v176 offset:38912
	ds_read_b128 v[226:229], v176 offset:39936
	s_mov_b32 m0, s83
	v_lshl_add_u64 v[230:231], v[246:247], 0, s[34:35]
	global_load_lds_dwordx4 v[230:231], off
	s_mov_b32 m0, s84
	v_lshl_add_u64 v[230:231], v[248:249], 0, s[34:35]
	global_load_lds_dwordx4 v[230:231], off
	s_waitcnt lgkmcnt(8)
	s_barrier
	s_waitcnt lgkmcnt(0)
	v_mfma_f32_16x16x32_f16 v[126:129], v[198:201], v[182:185], v[126:129]
	v_mfma_f32_16x16x32_f16 v[122:125], v[198:201], v[190:193], v[122:125]
	v_mfma_f32_16x16x32_f16 v[118:121], v[206:209], v[182:185], v[118:121]
	v_mfma_f32_16x16x32_f16 v[114:117], v[206:209], v[190:193], v[114:117]
	v_mfma_f32_16x16x32_f16 v[110:113], v[214:217], v[182:185], v[110:113]
	v_mfma_f32_16x16x32_f16 v[106:109], v[214:217], v[190:193], v[106:109]
	v_mfma_f32_16x16x32_f16 v[102:105], v[222:225], v[182:185], v[102:105]
	v_mfma_f32_16x16x32_f16 v[98:101], v[222:225], v[190:193], v[98:101]
	v_mfma_f32_16x16x32_f16 v[126:129], v[202:205], v[186:189], v[126:129]
	v_mfma_f32_16x16x32_f16 v[122:125], v[202:205], v[194:197], v[122:125]
	v_mfma_f32_16x16x32_f16 v[118:121], v[210:213], v[186:189], v[118:121]
	v_mfma_f32_16x16x32_f16 v[114:117], v[210:213], v[194:197], v[114:117]
	v_mfma_f32_16x16x32_f16 v[110:113], v[218:221], v[186:189], v[110:113]
	v_mfma_f32_16x16x32_f16 v[106:109], v[218:221], v[194:197], v[106:109]
	v_mfma_f32_16x16x32_f16 v[102:105], v[226:229], v[186:189], v[102:105]
	v_mfma_f32_16x16x32_f16 v[98:101], v[226:229], v[194:197], v[98:101]
	s_barrier
	v_lshl_add_u64 v[254:255], v[250:251], 0, s[36:37]
	s_mov_b32 m0, s85
	ds_read_b128 v[230:233], v150
	ds_read_b128 v[234:237], v151
	ds_read_b128 v[238:241], v152
	ds_read_b128 v[242:245], v153
	global_load_lds_dwordx4 v[254:255], off
	s_mov_b32 m0, s86
	v_lshl_add_u64 v[254:255], v[252:253], 0, s[36:37]
	global_load_lds_dwordx4 v[254:255], off
	s_barrier
	s_waitcnt lgkmcnt(0)
	v_mfma_f32_16x16x32_f16 v[94:97], v[198:201], v[230:233], v[94:97]
	v_mfma_f32_16x16x32_f16 v[90:93], v[198:201], v[238:241], v[90:93]
	v_mfma_f32_16x16x32_f16 v[86:89], v[206:209], v[230:233], v[86:89]
	v_mfma_f32_16x16x32_f16 v[82:85], v[206:209], v[238:241], v[82:85]
	v_mfma_f32_16x16x32_f16 v[78:81], v[214:217], v[230:233], v[78:81]
	v_mfma_f32_16x16x32_f16 v[74:77], v[214:217], v[238:241], v[74:77]
	v_mfma_f32_16x16x32_f16 v[70:73], v[222:225], v[230:233], v[70:73]
	v_mfma_f32_16x16x32_f16 v[66:69], v[222:225], v[238:241], v[66:69]
	v_mfma_f32_16x16x32_f16 v[94:97], v[202:205], v[234:237], v[94:97]
	v_mfma_f32_16x16x32_f16 v[90:93], v[202:205], v[242:245], v[90:93]
	v_mfma_f32_16x16x32_f16 v[86:89], v[210:213], v[234:237], v[86:89]
	v_mfma_f32_16x16x32_f16 v[82:85], v[210:213], v[242:245], v[82:85]
	v_mfma_f32_16x16x32_f16 v[78:81], v[218:221], v[234:237], v[78:81]
	v_mfma_f32_16x16x32_f16 v[74:77], v[218:221], v[242:245], v[74:77]
	v_mfma_f32_16x16x32_f16 v[70:73], v[226:229], v[234:237], v[70:73]
	v_mfma_f32_16x16x32_f16 v[66:69], v[226:229], v[242:245], v[66:69]
	v_lshl_add_u64 v[246:247], v[246:247], 0, s[36:37]
	s_mov_b32 m0, s87
	s_barrier
	ds_read_b128 v[198:201], v176 offset:49152
	ds_read_b128 v[202:205], v176 offset:50176
	ds_read_b128 v[206:209], v176 offset:51200
	ds_read_b128 v[210:213], v176 offset:52224
	ds_read_b128 v[214:217], v176 offset:53248
	ds_read_b128 v[218:221], v176 offset:54272
	ds_read_b128 v[222:225], v176 offset:55296
	ds_read_b128 v[226:229], v176 offset:56320
	global_load_lds_dwordx4 v[246:247], off
	s_mov_b32 m0, s88
	v_lshl_add_u64 v[246:247], v[248:249], 0, s[36:37]
	global_load_lds_dwordx4 v[246:247], off
	s_barrier
	s_waitcnt lgkmcnt(0)
	v_mfma_f32_16x16x32_f16 v[62:65], v[198:201], v[182:185], v[62:65]
	v_mfma_f32_16x16x32_f16 v[58:61], v[198:201], v[190:193], v[58:61]
	v_mfma_f32_16x16x32_f16 v[54:57], v[206:209], v[182:185], v[54:57]
	v_mfma_f32_16x16x32_f16 v[50:53], v[206:209], v[190:193], v[50:53]
	v_mfma_f32_16x16x32_f16 v[46:49], v[214:217], v[182:185], v[46:49]
	v_mfma_f32_16x16x32_f16 v[42:45], v[214:217], v[190:193], v[42:45]
	v_mfma_f32_16x16x32_f16 v[38:41], v[222:225], v[182:185], v[38:41]
	v_mfma_f32_16x16x32_f16 v[34:37], v[222:225], v[190:193], v[34:37]
	v_mfma_f32_16x16x32_f16 v[62:65], v[202:205], v[186:189], v[62:65]
	v_mfma_f32_16x16x32_f16 v[58:61], v[202:205], v[194:197], v[58:61]
	v_mfma_f32_16x16x32_f16 v[54:57], v[210:213], v[186:189], v[54:57]
	v_mfma_f32_16x16x32_f16 v[50:53], v[210:213], v[194:197], v[50:53]
	v_mfma_f32_16x16x32_f16 v[46:49], v[218:221], v[186:189], v[46:49]
	v_mfma_f32_16x16x32_f16 v[42:45], v[218:221], v[194:197], v[42:45]
	v_mfma_f32_16x16x32_f16 v[38:41], v[226:229], v[186:189], v[38:41]
	v_mfma_f32_16x16x32_f16 v[34:37], v[226:229], v[194:197], v[34:37]
	s_barrier
	s_mov_b32 m0, s89
	v_lshl_add_u64 v[182:183], v[250:251], 0, s[38:39]
	global_load_lds_dwordx4 v[182:183], off
	s_mov_b32 m0, s90
	v_lshl_add_u64 v[182:183], v[252:253], 0, s[38:39]
	global_load_lds_dwordx4 v[182:183], off
	s_waitcnt vmcnt(6)
	s_barrier
	v_mfma_f32_16x16x32_f16 v[30:33], v[198:201], v[230:233], v[30:33]
	v_mfma_f32_16x16x32_f16 v[26:29], v[198:201], v[238:241], v[26:29]
	v_mfma_f32_16x16x32_f16 v[22:25], v[206:209], v[230:233], v[22:25]
	v_mfma_f32_16x16x32_f16 v[18:21], v[206:209], v[238:241], v[18:21]
	v_mfma_f32_16x16x32_f16 v[14:17], v[214:217], v[230:233], v[14:17]
	v_mfma_f32_16x16x32_f16 v[10:13], v[214:217], v[238:241], v[10:13]
	v_mfma_f32_16x16x32_f16 v[6:9], v[222:225], v[230:233], v[6:9]
	v_mfma_f32_16x16x32_f16 v[2:5], v[222:225], v[238:241], v[2:5]
	v_mfma_f32_16x16x32_f16 v[30:33], v[202:205], v[234:237], v[30:33]
	v_mfma_f32_16x16x32_f16 v[26:29], v[202:205], v[242:245], v[26:29]
	v_mfma_f32_16x16x32_f16 v[22:25], v[210:213], v[234:237], v[22:25]
	v_mfma_f32_16x16x32_f16 v[18:21], v[210:213], v[242:245], v[18:21]
	v_mfma_f32_16x16x32_f16 v[14:17], v[218:221], v[234:237], v[14:17]
	v_mfma_f32_16x16x32_f16 v[10:13], v[218:221], v[242:245], v[10:13]
	v_mfma_f32_16x16x32_f16 v[6:9], v[226:229], v[234:237], v[6:9]
	v_mfma_f32_16x16x32_f16 v[2:5], v[226:229], v[242:245], v[2:5]
	s_add_i32 s46, s46, 2
	s_add_u32 s44, s44, 0x100
	s_addc_u32 s45, s45, 0
	s_cmp_lt_u32 s46, 4
	s_barrier
	s_cbranch_scc1 .LBB8_41
	s_add_u32 s42, s42, 0x20380
	s_addc_u32 s43, s43, 0
	v_readfirstlane_b32 s44, v177
	v_lshl_add_u64 v[130:131], v[130:131], 1, s[42:43]
	s_mov_b32 m0, s44
	ds_read_b128 v[134:137], v171
	ds_read_b128 v[138:141], v173
	ds_read_b128 v[154:157], v174
	ds_read_b128 v[168:171], v175
	ds_read_b128 v[182:185], v176
	ds_read_b128 v[186:189], v176 offset:1024
	ds_read_b128 v[190:193], v176 offset:2048
	ds_read_b128 v[194:197], v176 offset:3072
	ds_read_b128 v[198:201], v176 offset:4096
	ds_read_b128 v[202:205], v176 offset:5120
	ds_read_b128 v[206:209], v176 offset:6144
	ds_read_b128 v[210:213], v176 offset:7168
	global_load_lds_dwordx4 v[130:131], off
	v_lshl_add_u64 v[130:131], v[132:133], 1, s[42:43]
	v_readfirstlane_b32 s42, v178
	s_mov_b32 m0, s42
	s_nop 0
	global_load_lds_dwordx4 v[130:131], off
	s_barrier
	s_waitcnt lgkmcnt(0)
	v_mfma_f32_16x16x32_f16 v[122:125], v[182:185], v[154:157], v[122:125]
	v_mfma_f32_16x16x32_f16 v[110:113], v[198:201], v[134:137], v[110:113]
	v_mfma_f32_16x16x32_f16 v[98:101], v[206:209], v[154:157], v[98:101]
	v_mfma_f32_16x16x32_f16 v[126:129], v[182:185], v[134:137], v[126:129]
	v_mfma_f32_16x16x32_f16 v[122:125], v[186:189], v[168:171], v[122:125]
	v_mfma_f32_16x16x32_f16 v[118:121], v[190:193], v[134:137], v[118:121]
	v_mfma_f32_16x16x32_f16 v[114:117], v[190:193], v[154:157], v[114:117]
	v_mfma_f32_16x16x32_f16 v[130:133], v[202:205], v[138:141], v[110:113]
	v_mfma_f32_16x16x32_f16 v[106:109], v[198:201], v[154:157], v[106:109]
	v_mfma_f32_16x16x32_f16 v[102:105], v[206:209], v[134:137], v[102:105]
	v_mfma_f32_16x16x32_f16 v[98:101], v[210:213], v[168:171], v[98:101]
	v_mfma_f32_16x16x32_f16 v[126:129], v[186:189], v[138:141], v[126:129]
	v_mfma_f32_16x16x32_f16 v[118:121], v[194:197], v[138:141], v[118:121]
	v_mfma_f32_16x16x32_f16 v[114:117], v[194:197], v[168:171], v[114:117]
	v_mfma_f32_16x16x32_f16 v[214:217], v[202:205], v[168:171], v[106:109]
	v_mfma_f32_16x16x32_f16 v[102:105], v[210:213], v[138:141], v[102:105]
	s_barrier
	ds_read_b128 v[106:109], v162
	ds_read_b128 v[110:113], v163
	ds_read_b128 v[160:163], v164
	ds_read_b128 v[218:221], v165
	s_barrier
	s_waitcnt lgkmcnt(0)
	v_mfma_f32_16x16x32_f16 v[82:85], v[190:193], v[160:163], v[82:85]
	v_mfma_f32_16x16x32_f16 v[78:81], v[198:201], v[106:109], v[78:81]
	v_mfma_f32_16x16x32_f16 v[74:77], v[198:201], v[160:163], v[74:77]
	v_mfma_f32_16x16x32_f16 v[70:73], v[206:209], v[106:109], v[70:73]
	v_mfma_f32_16x16x32_f16 v[66:69], v[206:209], v[160:163], v[66:69]
	v_mfma_f32_16x16x32_f16 v[94:97], v[182:185], v[106:109], v[94:97]
	v_mfma_f32_16x16x32_f16 v[90:93], v[182:185], v[160:163], v[90:93]
	v_mfma_f32_16x16x32_f16 v[86:89], v[190:193], v[106:109], v[86:89]
	v_mfma_f32_16x16x32_f16 v[82:85], v[194:197], v[218:221], v[82:85]
	v_mfma_f32_16x16x32_f16 v[78:81], v[202:205], v[110:113], v[78:81]
	v_mfma_f32_16x16x32_f16 v[74:77], v[202:205], v[218:221], v[74:77]
	v_mfma_f32_16x16x32_f16 v[70:73], v[210:213], v[110:113], v[70:73]
	v_mfma_f32_16x16x32_f16 v[66:69], v[210:213], v[218:221], v[66:69]
	v_mfma_f32_16x16x32_f16 v[222:225], v[186:189], v[110:113], v[94:97]
	v_mfma_f32_16x16x32_f16 v[182:185], v[186:189], v[218:221], v[90:93]
	v_mfma_f32_16x16x32_f16 v[86:89], v[194:197], v[110:113], v[86:89]
	s_barrier
	ds_read_b128 v[90:93], v176 offset:16384
	ds_read_b128 v[94:97], v176 offset:17408
	ds_read_b128 v[186:189], v176 offset:18432
	ds_read_b128 v[190:193], v176 offset:19456
	ds_read_b128 v[194:197], v176 offset:20480
	ds_read_b128 v[198:201], v176 offset:21504
	ds_read_b128 v[202:205], v176 offset:22528
	ds_read_b128 v[206:209], v176 offset:23552
	s_waitcnt vmcnt(4)
	s_barrier
	s_waitcnt lgkmcnt(0)
	v_mfma_f32_16x16x32_f16 v[46:49], v[194:197], v[134:137], v[46:49]
	v_mfma_f32_16x16x32_f16 v[42:45], v[194:197], v[154:157], v[42:45]
	v_mfma_f32_16x16x32_f16 v[38:41], v[202:205], v[134:137], v[38:41]
	v_mfma_f32_16x16x32_f16 v[34:37], v[202:205], v[154:157], v[34:37]
	v_mfma_f32_16x16x32_f16 v[62:65], v[90:93], v[134:137], v[62:65]
	v_mfma_f32_16x16x32_f16 v[58:61], v[90:93], v[154:157], v[58:61]
	v_mfma_f32_16x16x32_f16 v[54:57], v[186:189], v[134:137], v[54:57]
	v_mfma_f32_16x16x32_f16 v[50:53], v[186:189], v[154:157], v[50:53]
	v_mfma_f32_16x16x32_f16 v[46:49], v[198:201], v[138:141], v[46:49]
	v_mfma_f32_16x16x32_f16 v[42:45], v[198:201], v[168:171], v[42:45]
	v_mfma_f32_16x16x32_f16 v[38:41], v[206:209], v[138:141], v[38:41]
	v_mfma_f32_16x16x32_f16 v[34:37], v[206:209], v[168:171], v[34:37]
	v_mfma_f32_16x16x32_f16 v[210:213], v[94:97], v[138:141], v[62:65]
	v_mfma_f32_16x16x32_f16 v[226:229], v[94:97], v[168:171], v[58:61]
	v_mfma_f32_16x16x32_f16 v[230:233], v[190:193], v[138:141], v[54:57]
	v_mfma_f32_16x16x32_f16 v[234:237], v[190:193], v[168:171], v[50:53]
	v_mfma_f32_16x16x32_f16 v[2:5], v[202:205], v[160:163], v[2:5]
	v_mfma_f32_16x16x32_f16 v[30:33], v[90:93], v[106:109], v[30:33]
	v_mfma_f32_16x16x32_f16 v[26:29], v[90:93], v[160:163], v[26:29]
	v_mfma_f32_16x16x32_f16 v[22:25], v[186:189], v[106:109], v[22:25]
	v_mfma_f32_16x16x32_f16 v[18:21], v[186:189], v[160:163], v[18:21]
	v_mfma_f32_16x16x32_f16 v[14:17], v[194:197], v[106:109], v[14:17]
	v_mfma_f32_16x16x32_f16 v[10:13], v[194:197], v[160:163], v[10:13]
	v_mfma_f32_16x16x32_f16 v[6:9], v[202:205], v[106:109], v[6:9]
	v_mfma_f32_16x16x32_f16 v[2:5], v[206:209], v[218:221], v[2:5]
	v_mfma_f32_16x16x32_f16 v[138:141], v[94:97], v[110:113], v[30:33]
	v_mfma_f32_16x16x32_f16 v[168:171], v[94:97], v[218:221], v[26:29]
	v_mfma_f32_16x16x32_f16 v[238:241], v[190:193], v[110:113], v[22:25]
	v_mfma_f32_16x16x32_f16 v[186:189], v[190:193], v[218:221], v[18:21]
	v_mfma_f32_16x16x32_f16 v[190:193], v[198:201], v[110:113], v[14:17]
	v_mfma_f32_16x16x32_f16 v[194:197], v[198:201], v[218:221], v[10:13]
	v_mfma_f32_16x16x32_f16 v[198:201], v[206:209], v[110:113], v[6:9]
	s_barrier
	s_nop 0
	ds_read_b128 v[6:9], v144
	ds_read_b128 v[10:13], v145
	ds_read_b128 v[14:17], v146
	ds_read_b128 v[160:163], v147
	ds_read_b128 v[18:21], v176 offset:32768
	ds_read_b128 v[22:25], v176 offset:33792
	ds_read_b128 v[26:29], v176 offset:34816
	ds_read_b128 v[50:53], v176 offset:35840
	ds_read_b128 v[202:205], v176 offset:36864
	ds_read_b128 v[206:209], v176 offset:37888
	ds_read_b128 v[218:221], v176 offset:38912
	ds_read_b128 v[242:245], v176 offset:39936
	s_waitcnt vmcnt(2)
	s_barrier
	s_waitcnt lgkmcnt(0)
	v_mfma_f32_16x16x32_f16 v[30:33], v[18:21], v[6:9], v[126:129]
	v_mfma_f32_16x16x32_f16 v[154:157], v[22:25], v[10:13], v[30:33]
	v_mfma_f32_16x16x32_f16 v[30:33], v[18:21], v[14:17], v[122:125]
	v_mfma_f32_16x16x32_f16 v[110:113], v[22:25], v[160:163], v[30:33]
	v_mfma_f32_16x16x32_f16 v[30:33], v[26:29], v[6:9], v[118:121]
	v_mfma_f32_16x16x32_f16 v[146:149], v[50:53], v[10:13], v[30:33]
	v_mfma_f32_16x16x32_f16 v[30:33], v[26:29], v[14:17], v[114:117]
	v_mfma_f32_16x16x32_f16 v[106:109], v[50:53], v[160:163], v[30:33]
	v_mfma_f32_16x16x32_f16 v[30:33], v[202:205], v[6:9], v[130:133]
	v_mfma_f32_16x16x32_f16 v[142:145], v[206:209], v[10:13], v[30:33]
	v_mfma_f32_16x16x32_f16 v[30:33], v[202:205], v[14:17], v[214:217]
	v_mfma_f32_16x16x32_f16 v[94:97], v[206:209], v[160:163], v[30:33]
	v_mfma_f32_16x16x32_f16 v[30:33], v[218:221], v[6:9], v[102:105]
	v_mfma_f32_16x16x32_f16 v[134:137], v[242:245], v[10:13], v[30:33]
	v_mfma_f32_16x16x32_f16 v[30:33], v[218:221], v[14:17], v[98:101]
	v_mfma_f32_16x16x32_f16 v[90:93], v[242:245], v[160:163], v[30:33]
	s_barrier
	ds_read_b128 v[102:105], v150
	ds_read_b128 v[114:117], v151
	ds_read_b128 v[118:121], v152
	ds_read_b128 v[126:129], v153
	s_waitcnt vmcnt(0)
	s_barrier
	s_waitcnt lgkmcnt(0)
	v_mfma_f32_16x16x32_f16 v[30:33], v[18:21], v[102:105], v[222:225]
	v_mfma_f32_16x16x32_f16 v[18:21], v[18:21], v[118:121], v[182:185]
	v_mfma_f32_16x16x32_f16 v[62:65], v[22:25], v[114:117], v[30:33]
	v_mfma_f32_16x16x32_f16 v[30:33], v[22:25], v[126:129], v[18:21]
	v_mfma_f32_16x16x32_f16 v[18:21], v[26:29], v[102:105], v[86:89]
	v_mfma_f32_16x16x32_f16 v[58:61], v[50:53], v[114:117], v[18:21]
	v_mfma_f32_16x16x32_f16 v[18:21], v[26:29], v[118:121], v[82:85]
	v_mfma_f32_16x16x32_f16 v[26:29], v[50:53], v[126:129], v[18:21]
	v_mfma_f32_16x16x32_f16 v[18:21], v[202:205], v[102:105], v[78:81]
	v_mfma_f32_16x16x32_f16 v[54:57], v[206:209], v[114:117], v[18:21]
	v_mfma_f32_16x16x32_f16 v[18:21], v[202:205], v[118:121], v[74:77]
	v_mfma_f32_16x16x32_f16 v[22:25], v[206:209], v[126:129], v[18:21]
	v_mfma_f32_16x16x32_f16 v[18:21], v[218:221], v[102:105], v[70:73]
	v_mfma_f32_16x16x32_f16 v[50:53], v[242:245], v[114:117], v[18:21]
	v_mfma_f32_16x16x32_f16 v[18:21], v[218:221], v[118:121], v[66:69]
	v_mfma_f32_16x16x32_f16 v[18:21], v[242:245], v[126:129], v[18:21]
	s_barrier
	ds_read_b128 v[86:89], v176 offset:49152
	ds_read_b128 v[150:153], v176 offset:50176
	ds_read_b128 v[182:185], v176 offset:51200
	ds_read_b128 v[202:205], v176 offset:52224
	ds_read_b128 v[206:209], v176 offset:53248
	ds_read_b128 v[214:217], v176 offset:54272
	ds_read_b128 v[218:221], v176 offset:55296
	ds_read_b128 v[174:177], v176 offset:56320
	s_barrier
	s_waitcnt lgkmcnt(0)
	v_mfma_f32_16x16x32_f16 v[66:69], v[86:89], v[6:9], v[210:213]
	v_mfma_f32_16x16x32_f16 v[130:133], v[150:153], v[10:13], v[66:69]
	v_mfma_f32_16x16x32_f16 v[66:69], v[86:89], v[14:17], v[226:229]
	v_mfma_f32_16x16x32_f16 v[78:81], v[150:153], v[160:163], v[66:69]
	v_mfma_f32_16x16x32_f16 v[66:69], v[182:185], v[6:9], v[230:233]
	v_mfma_f32_16x16x32_f16 v[46:49], v[206:209], v[6:9], v[46:49]
	v_mfma_f32_16x16x32_f16 v[6:9], v[218:221], v[6:9], v[38:41]
	v_mfma_f32_16x16x32_f16 v[122:125], v[202:205], v[10:13], v[66:69]
	v_mfma_f32_16x16x32_f16 v[66:69], v[182:185], v[14:17], v[234:237]
	v_mfma_f32_16x16x32_f16 v[42:45], v[206:209], v[14:17], v[42:45]
	v_mfma_f32_16x16x32_f16 v[82:85], v[174:177], v[10:13], v[6:9]
	v_mfma_f32_16x16x32_f16 v[6:9], v[218:221], v[14:17], v[34:37]
	v_mfma_f32_16x16x32_f16 v[74:77], v[202:205], v[160:163], v[66:69]
	v_mfma_f32_16x16x32_f16 v[98:101], v[214:217], v[10:13], v[46:49]
	v_mfma_f32_16x16x32_f16 v[70:73], v[214:217], v[160:163], v[42:45]
	v_mfma_f32_16x16x32_f16 v[66:69], v[174:177], v[160:163], v[6:9]
	v_mfma_f32_16x16x32_f16 v[6:9], v[86:89], v[102:105], v[138:141]
	v_mfma_f32_16x16x32_f16 v[46:49], v[150:153], v[114:117], v[6:9]
	v_mfma_f32_16x16x32_f16 v[6:9], v[86:89], v[118:121], v[168:171]
	v_mfma_f32_16x16x32_f16 v[14:17], v[150:153], v[126:129], v[6:9]
	v_mfma_f32_16x16x32_f16 v[6:9], v[182:185], v[102:105], v[238:241]
	v_mfma_f32_16x16x32_f16 v[42:45], v[202:205], v[114:117], v[6:9]
	v_mfma_f32_16x16x32_f16 v[6:9], v[182:185], v[118:121], v[186:189]
	v_mfma_f32_16x16x32_f16 v[10:13], v[202:205], v[126:129], v[6:9]
	v_mfma_f32_16x16x32_f16 v[6:9], v[206:209], v[102:105], v[190:193]
	v_mfma_f32_16x16x32_f16 v[38:41], v[214:217], v[114:117], v[6:9]
	v_mfma_f32_16x16x32_f16 v[6:9], v[206:209], v[118:121], v[194:197]
	v_mfma_f32_16x16x32_f16 v[34:37], v[218:221], v[102:105], v[198:201]
	v_mfma_f32_16x16x32_f16 v[2:5], v[218:221], v[118:121], v[2:5]
	v_mfma_f32_16x16x32_f16 v[6:9], v[214:217], v[126:129], v[6:9]
	v_mfma_f32_16x16x32_f16 v[34:37], v[174:177], v[114:117], v[34:37]
	v_mfma_f32_16x16x32_f16 v[2:5], v[174:177], v[126:129], v[2:5]
	s_cmpk_gt_u32 s62, 0xff
	s_barrier
	s_cbranch_scc1 .LBB8_44
	s_barrier

.LBB9_38:
	ds_read_b128 v[176:179], v169
	ds_read_b128 v[180:183], v170
	ds_read_b128 v[184:187], v171
	ds_read_b128 v[188:191], v172
	v_add_u32_e32 v174, 0xc000, v152
	v_lshl_add_u64 v[192:193], v[136:137], 0, s[42:43]
	v_add_u32_e32 v175, 0xe000, v152
	v_add_u32_e32 v173, s39, v168
	ds_read_b128 v[198:201], v173
	ds_read_b128 v[202:205], v173 offset:1024
	ds_read_b128 v[206:209], v173 offset:2048
	ds_read_b128 v[210:213], v173 offset:3072
	ds_read_b128 v[214:217], v173 offset:4096
	ds_read_b128 v[218:221], v173 offset:5120
	ds_read_b128 v[222:225], v173 offset:6144
	ds_read_b128 v[226:229], v173 offset:7168
	v_lshl_add_u64 v[230:231], v[192:193], 0, s[10:11]
	s_mov_b32 m0, s65
	v_lshl_add_u64 v[246:247], v[134:135], 0, s[42:43]
	global_load_lds_dwordx4 v[230:231], off
	s_mov_b32 m0, s66
	v_lshl_add_u64 v[230:231], v[246:247], 0, s[10:11]
	global_load_lds_dwordx4 v[230:231], off
	s_waitcnt lgkmcnt(8)
	s_barrier
	s_waitcnt lgkmcnt(0)
	v_mfma_f32_16x16x32_f16 v[2:5], v[198:201], v[176:179], v[2:5]
	v_mfma_f32_16x16x32_f16 v[6:9], v[198:201], v[184:187], v[6:9]
	v_mfma_f32_16x16x32_f16 v[10:13], v[206:209], v[176:179], v[10:13]
	v_mfma_f32_16x16x32_f16 v[18:21], v[206:209], v[184:187], v[18:21]
	v_mfma_f32_16x16x32_f16 v[30:33], v[214:217], v[176:179], v[30:33]
	v_mfma_f32_16x16x32_f16 v[42:45], v[214:217], v[184:187], v[42:45]
	v_mfma_f32_16x16x32_f16 v[54:57], v[222:225], v[176:179], v[54:57]
	v_mfma_f32_16x16x32_f16 v[66:69], v[222:225], v[184:187], v[66:69]
	v_mfma_f32_16x16x32_f16 v[2:5], v[202:205], v[180:183], v[2:5]
	v_mfma_f32_16x16x32_f16 v[6:9], v[202:205], v[188:191], v[6:9]
	v_mfma_f32_16x16x32_f16 v[10:13], v[210:213], v[180:183], v[10:13]
	v_mfma_f32_16x16x32_f16 v[18:21], v[210:213], v[188:191], v[18:21]
	v_mfma_f32_16x16x32_f16 v[30:33], v[218:221], v[180:183], v[30:33]
	v_mfma_f32_16x16x32_f16 v[42:45], v[218:221], v[188:191], v[42:45]
	v_mfma_f32_16x16x32_f16 v[54:57], v[226:229], v[180:183], v[54:57]
	v_mfma_f32_16x16x32_f16 v[66:69], v[226:229], v[188:191], v[66:69]
	s_barrier
	v_lshl_add_u64 v[248:249], v[140:141], 0, s[42:43]
	v_lshl_add_u64 v[250:251], v[248:249], 0, s[26:27]
	s_mov_b32 m0, s67
	ds_read_b128 v[230:233], v161
	ds_read_b128 v[234:237], v162
	ds_read_b128 v[238:241], v163
	ds_read_b128 v[242:245], v164
	global_load_lds_dwordx4 v[250:251], off
	v_lshl_add_u64 v[250:251], v[138:139], 0, s[42:43]
	s_mov_b32 m0, s68
	v_lshl_add_u64 v[252:253], v[250:251], 0, s[26:27]
	global_load_lds_dwordx4 v[252:253], off
	s_barrier
	s_waitcnt lgkmcnt(0)
	v_mfma_f32_16x16x32_f16 v[14:17], v[198:201], v[230:233], v[14:17]
	v_mfma_f32_16x16x32_f16 v[22:25], v[198:201], v[238:241], v[22:25]
	v_mfma_f32_16x16x32_f16 v[34:37], v[206:209], v[230:233], v[34:37]
	v_mfma_f32_16x16x32_f16 v[46:49], v[206:209], v[238:241], v[46:49]
	v_mfma_f32_16x16x32_f16 v[58:61], v[214:217], v[230:233], v[58:61]
	v_mfma_f32_16x16x32_f16 v[70:73], v[214:217], v[238:241], v[70:73]
	v_mfma_f32_16x16x32_f16 v[78:81], v[222:225], v[230:233], v[78:81]
	v_mfma_f32_16x16x32_f16 v[86:89], v[222:225], v[238:241], v[86:89]
	v_mfma_f32_16x16x32_f16 v[14:17], v[202:205], v[234:237], v[14:17]
	v_mfma_f32_16x16x32_f16 v[22:25], v[202:205], v[242:245], v[22:25]
	v_mfma_f32_16x16x32_f16 v[34:37], v[210:213], v[234:237], v[34:37]
	v_mfma_f32_16x16x32_f16 v[46:49], v[210:213], v[242:245], v[46:49]
	v_mfma_f32_16x16x32_f16 v[58:61], v[218:221], v[234:237], v[58:61]
	v_mfma_f32_16x16x32_f16 v[70:73], v[218:221], v[242:245], v[70:73]
	v_mfma_f32_16x16x32_f16 v[78:81], v[226:229], v[234:237], v[78:81]
	v_mfma_f32_16x16x32_f16 v[86:89], v[226:229], v[242:245], v[86:89]
	v_lshl_add_u64 v[252:253], v[192:193], 0, s[26:27]
	s_mov_b32 m0, s69
	s_barrier
	ds_read_b128 v[198:201], v173 offset:16384
	ds_read_b128 v[202:205], v173 offset:17408
	ds_read_b128 v[206:209], v173 offset:18432
	ds_read_b128 v[210:213], v173 offset:19456
	ds_read_b128 v[214:217], v173 offset:20480
	ds_read_b128 v[218:221], v173 offset:21504
	ds_read_b128 v[222:225], v173 offset:22528
	ds_read_b128 v[226:229], v173 offset:23552
	global_load_lds_dwordx4 v[252:253], off
	s_mov_b32 m0, s70
	v_lshl_add_u64 v[252:253], v[246:247], 0, s[26:27]
	global_load_lds_dwordx4 v[252:253], off
	s_barrier
	s_waitcnt lgkmcnt(0)
	v_mfma_f32_16x16x32_f16 v[26:29], v[198:201], v[176:179], v[26:29]
	v_mfma_f32_16x16x32_f16 v[38:41], v[198:201], v[184:187], v[38:41]
	v_mfma_f32_16x16x32_f16 v[50:53], v[206:209], v[176:179], v[50:53]
	v_mfma_f32_16x16x32_f16 v[62:65], v[206:209], v[184:187], v[62:65]
	v_mfma_f32_16x16x32_f16 v[74:77], v[214:217], v[176:179], v[74:77]
	v_mfma_f32_16x16x32_f16 v[82:85], v[214:217], v[184:187], v[82:85]
	v_mfma_f32_16x16x32_f16 v[90:93], v[222:225], v[176:179], v[90:93]
	v_mfma_f32_16x16x32_f16 v[94:97], v[222:225], v[184:187], v[94:97]
	v_mfma_f32_16x16x32_f16 v[26:29], v[202:205], v[180:183], v[26:29]
	v_mfma_f32_16x16x32_f16 v[38:41], v[202:205], v[188:191], v[38:41]
	v_mfma_f32_16x16x32_f16 v[50:53], v[210:213], v[180:183], v[50:53]
	v_mfma_f32_16x16x32_f16 v[62:65], v[210:213], v[188:191], v[62:65]
	v_mfma_f32_16x16x32_f16 v[74:77], v[218:221], v[180:183], v[74:77]
	v_mfma_f32_16x16x32_f16 v[82:85], v[218:221], v[188:191], v[82:85]
	v_mfma_f32_16x16x32_f16 v[90:93], v[226:229], v[180:183], v[90:93]
	v_mfma_f32_16x16x32_f16 v[94:97], v[226:229], v[188:191], v[94:97]
	s_barrier
	s_mov_b32 m0, s71
	v_lshl_add_u64 v[176:177], v[248:249], 0, s[28:29]
	global_load_lds_dwordx4 v[176:177], off
	s_mov_b32 m0, s72
	v_lshl_add_u64 v[176:177], v[250:251], 0, s[28:29]
	global_load_lds_dwordx4 v[176:177], off
	s_waitcnt vmcnt(6)
	s_barrier
	v_mfma_f32_16x16x32_f16 v[98:101], v[198:201], v[230:233], v[98:101]
	v_mfma_f32_16x16x32_f16 v[102:105], v[198:201], v[238:241], v[102:105]
	v_mfma_f32_16x16x32_f16 v[106:109], v[206:209], v[230:233], v[106:109]
	v_mfma_f32_16x16x32_f16 v[110:113], v[206:209], v[238:241], v[110:113]
	v_mfma_f32_16x16x32_f16 v[114:117], v[214:217], v[230:233], v[114:117]
	v_mfma_f32_16x16x32_f16 v[118:121], v[214:217], v[238:241], v[118:121]
	v_mfma_f32_16x16x32_f16 v[122:125], v[222:225], v[230:233], v[122:125]
	v_mfma_f32_16x16x32_f16 v[126:129], v[222:225], v[238:241], v[126:129]
	v_mfma_f32_16x16x32_f16 v[98:101], v[202:205], v[234:237], v[98:101]
	v_mfma_f32_16x16x32_f16 v[102:105], v[202:205], v[242:245], v[102:105]
	v_mfma_f32_16x16x32_f16 v[106:109], v[210:213], v[234:237], v[106:109]
	v_mfma_f32_16x16x32_f16 v[110:113], v[210:213], v[242:245], v[110:113]
	v_mfma_f32_16x16x32_f16 v[114:117], v[218:221], v[234:237], v[114:117]
	v_mfma_f32_16x16x32_f16 v[118:121], v[218:221], v[242:245], v[118:121]
	v_mfma_f32_16x16x32_f16 v[122:125], v[226:229], v[234:237], v[122:125]
	v_mfma_f32_16x16x32_f16 v[126:129], v[226:229], v[242:245], v[126:129]
	s_barrier
	ds_read_b128 v[176:179], v144
	ds_read_b128 v[180:183], v145
	ds_read_b128 v[184:187], v150
	ds_read_b128 v[188:191], v151
	ds_read_b128 v[198:201], v173 offset:32768
	ds_read_b128 v[202:205], v173 offset:33792
	ds_read_b128 v[206:209], v173 offset:34816
	ds_read_b128 v[210:213], v173 offset:35840
	ds_read_b128 v[214:217], v173 offset:36864
	ds_read_b128 v[218:221], v173 offset:37888
	ds_read_b128 v[222:225], v173 offset:38912
	ds_read_b128 v[226:229], v173 offset:39936
	s_mov_b32 m0, s73
	v_lshl_add_u64 v[230:231], v[192:193], 0, s[28:29]
	global_load_lds_dwordx4 v[230:231], off
	s_mov_b32 m0, s74
	v_lshl_add_u64 v[230:231], v[246:247], 0, s[28:29]
	global_load_lds_dwordx4 v[230:231], off
	s_waitcnt lgkmcnt(8)
	s_barrier
	s_waitcnt lgkmcnt(0)
	v_mfma_f32_16x16x32_f16 v[2:5], v[198:201], v[176:179], v[2:5]
	v_mfma_f32_16x16x32_f16 v[6:9], v[198:201], v[184:187], v[6:9]
	v_mfma_f32_16x16x32_f16 v[10:13], v[206:209], v[176:179], v[10:13]
	v_mfma_f32_16x16x32_f16 v[18:21], v[206:209], v[184:187], v[18:21]
	v_mfma_f32_16x16x32_f16 v[30:33], v[214:217], v[176:179], v[30:33]
	v_mfma_f32_16x16x32_f16 v[42:45], v[214:217], v[184:187], v[42:45]
	v_mfma_f32_16x16x32_f16 v[54:57], v[222:225], v[176:179], v[54:57]
	v_mfma_f32_16x16x32_f16 v[66:69], v[222:225], v[184:187], v[66:69]
	v_mfma_f32_16x16x32_f16 v[2:5], v[202:205], v[180:183], v[2:5]
	v_mfma_f32_16x16x32_f16 v[6:9], v[202:205], v[188:191], v[6:9]
	v_mfma_f32_16x16x32_f16 v[10:13], v[210:213], v[180:183], v[10:13]
	v_mfma_f32_16x16x32_f16 v[18:21], v[210:213], v[188:191], v[18:21]
	v_mfma_f32_16x16x32_f16 v[30:33], v[218:221], v[180:183], v[30:33]
	v_mfma_f32_16x16x32_f16 v[42:45], v[218:221], v[188:191], v[42:45]
	v_mfma_f32_16x16x32_f16 v[54:57], v[226:229], v[180:183], v[54:57]
	v_mfma_f32_16x16x32_f16 v[66:69], v[226:229], v[188:191], v[66:69]
	s_barrier
	v_lshl_add_u64 v[252:253], v[248:249], 0, s[30:31]
	s_mov_b32 m0, s75
	ds_read_b128 v[230:233], v146
	ds_read_b128 v[234:237], v147
	ds_read_b128 v[238:241], v148
	ds_read_b128 v[242:245], v149
	global_load_lds_dwordx4 v[252:253], off
	s_mov_b32 m0, s76
	v_lshl_add_u64 v[252:253], v[250:251], 0, s[30:31]
	global_load_lds_dwordx4 v[252:253], off
	s_barrier
	s_waitcnt lgkmcnt(0)
	v_mfma_f32_16x16x32_f16 v[14:17], v[198:201], v[230:233], v[14:17]
	v_mfma_f32_16x16x32_f16 v[22:25], v[198:201], v[238:241], v[22:25]
	v_mfma_f32_16x16x32_f16 v[34:37], v[206:209], v[230:233], v[34:37]
	v_mfma_f32_16x16x32_f16 v[46:49], v[206:209], v[238:241], v[46:49]
	v_mfma_f32_16x16x32_f16 v[58:61], v[214:217], v[230:233], v[58:61]
	v_mfma_f32_16x16x32_f16 v[70:73], v[214:217], v[238:241], v[70:73]
	v_mfma_f32_16x16x32_f16 v[78:81], v[222:225], v[230:233], v[78:81]
	v_mfma_f32_16x16x32_f16 v[86:89], v[222:225], v[238:241], v[86:89]
	v_mfma_f32_16x16x32_f16 v[14:17], v[202:205], v[234:237], v[14:17]
	v_mfma_f32_16x16x32_f16 v[22:25], v[202:205], v[242:245], v[22:25]
	v_mfma_f32_16x16x32_f16 v[34:37], v[210:213], v[234:237], v[34:37]
	v_mfma_f32_16x16x32_f16 v[46:49], v[210:213], v[242:245], v[46:49]
	v_mfma_f32_16x16x32_f16 v[58:61], v[218:221], v[234:237], v[58:61]
	v_mfma_f32_16x16x32_f16 v[70:73], v[218:221], v[242:245], v[70:73]
	v_mfma_f32_16x16x32_f16 v[78:81], v[226:229], v[234:237], v[78:81]
	v_mfma_f32_16x16x32_f16 v[86:89], v[226:229], v[242:245], v[86:89]
	v_lshl_add_u64 v[192:193], v[192:193], 0, s[30:31]
	s_mov_b32 m0, s77
	s_barrier
	ds_read_b128 v[198:201], v173 offset:49152
	ds_read_b128 v[202:205], v173 offset:50176
	ds_read_b128 v[206:209], v173 offset:51200
	ds_read_b128 v[210:213], v173 offset:52224
	ds_read_b128 v[214:217], v173 offset:53248
	ds_read_b128 v[218:221], v173 offset:54272
	ds_read_b128 v[222:225], v173 offset:55296
	ds_read_b128 v[226:229], v173 offset:56320
	global_load_lds_dwordx4 v[192:193], off
	s_mov_b32 m0, s78
	v_lshl_add_u64 v[192:193], v[246:247], 0, s[30:31]
	global_load_lds_dwordx4 v[192:193], off
	s_barrier
	s_waitcnt lgkmcnt(0)
	v_mfma_f32_16x16x32_f16 v[26:29], v[198:201], v[176:179], v[26:29]
	v_mfma_f32_16x16x32_f16 v[38:41], v[198:201], v[184:187], v[38:41]
	v_mfma_f32_16x16x32_f16 v[50:53], v[206:209], v[176:179], v[50:53]
	v_mfma_f32_16x16x32_f16 v[62:65], v[206:209], v[184:187], v[62:65]
	v_mfma_f32_16x16x32_f16 v[74:77], v[214:217], v[176:179], v[74:77]
	v_mfma_f32_16x16x32_f16 v[82:85], v[214:217], v[184:187], v[82:85]
	v_mfma_f32_16x16x32_f16 v[90:93], v[222:225], v[176:179], v[90:93]
	v_mfma_f32_16x16x32_f16 v[94:97], v[222:225], v[184:187], v[94:97]
	v_mfma_f32_16x16x32_f16 v[26:29], v[202:205], v[180:183], v[26:29]
	v_mfma_f32_16x16x32_f16 v[38:41], v[202:205], v[188:191], v[38:41]
	v_mfma_f32_16x16x32_f16 v[50:53], v[210:213], v[180:183], v[50:53]
	v_mfma_f32_16x16x32_f16 v[62:65], v[210:213], v[188:191], v[62:65]
	v_mfma_f32_16x16x32_f16 v[74:77], v[218:221], v[180:183], v[74:77]
	v_mfma_f32_16x16x32_f16 v[82:85], v[218:221], v[188:191], v[82:85]
	v_mfma_f32_16x16x32_f16 v[90:93], v[226:229], v[180:183], v[90:93]
	v_mfma_f32_16x16x32_f16 v[94:97], v[226:229], v[188:191], v[94:97]
	s_barrier
	s_mov_b32 m0, s79
	v_lshl_add_u64 v[176:177], v[248:249], 0, s[34:35]
	global_load_lds_dwordx4 v[176:177], off
	s_mov_b32 m0, s80
	v_lshl_add_u64 v[176:177], v[250:251], 0, s[34:35]
	global_load_lds_dwordx4 v[176:177], off
	s_waitcnt vmcnt(6)
	s_barrier
	v_mfma_f32_16x16x32_f16 v[98:101], v[198:201], v[230:233], v[98:101]
	v_mfma_f32_16x16x32_f16 v[102:105], v[198:201], v[238:241], v[102:105]
	v_mfma_f32_16x16x32_f16 v[106:109], v[206:209], v[230:233], v[106:109]
	v_mfma_f32_16x16x32_f16 v[110:113], v[206:209], v[238:241], v[110:113]
	v_mfma_f32_16x16x32_f16 v[114:117], v[214:217], v[230:233], v[114:117]
	v_mfma_f32_16x16x32_f16 v[118:121], v[214:217], v[238:241], v[118:121]
	v_mfma_f32_16x16x32_f16 v[122:125], v[222:225], v[230:233], v[122:125]
	v_mfma_f32_16x16x32_f16 v[126:129], v[222:225], v[238:241], v[126:129]
	v_mfma_f32_16x16x32_f16 v[98:101], v[202:205], v[234:237], v[98:101]
	v_mfma_f32_16x16x32_f16 v[102:105], v[202:205], v[242:245], v[102:105]
	v_mfma_f32_16x16x32_f16 v[106:109], v[210:213], v[234:237], v[106:109]
	v_mfma_f32_16x16x32_f16 v[110:113], v[210:213], v[242:245], v[110:113]
	v_mfma_f32_16x16x32_f16 v[114:117], v[218:221], v[234:237], v[114:117]
	v_mfma_f32_16x16x32_f16 v[118:121], v[218:221], v[242:245], v[118:121]
	v_mfma_f32_16x16x32_f16 v[122:125], v[226:229], v[234:237], v[122:125]
	v_mfma_f32_16x16x32_f16 v[126:129], v[226:229], v[242:245], v[126:129]
	s_add_i32 s44, s44, 2
	s_add_u32 s42, s42, 0x100
	s_addc_u32 s43, s43, 0
	s_cmp_lt_u32 s44, 4
	s_barrier
	s_cbranch_scc1 .LBB9_38
	s_add_u32 s40, s40, 0x20380
	s_addc_u32 s41, s41, 0
	v_readfirstlane_b32 s39, v174
	v_lshl_add_u64 v[130:131], v[130:131], 1, s[40:41]
	s_mov_b32 m0, s39
	v_readfirstlane_b32 s39, v175
	ds_read_b128 v[134:137], v169
	ds_read_b128 v[138:141], v170
	ds_read_b128 v[152:155], v171
	ds_read_b128 v[156:159], v172
	ds_read_b128 v[166:169], v173
	ds_read_b128 v[176:179], v173 offset:1024
	ds_read_b128 v[180:183], v173 offset:2048
	ds_read_b128 v[184:187], v173 offset:3072
	ds_read_b128 v[188:191], v173 offset:4096
	ds_read_b128 v[198:201], v173 offset:5120
	ds_read_b128 v[202:205], v173 offset:6144
	ds_read_b128 v[206:209], v173 offset:7168
	global_load_lds_dwordx4 v[130:131], off
	s_mov_b32 m0, s39
	v_lshl_add_u64 v[130:131], v[132:133], 1, s[40:41]
	global_load_lds_dwordx4 v[130:131], off
	s_barrier
	s_waitcnt lgkmcnt(0)
	v_mfma_f32_16x16x32_f16 v[2:5], v[166:169], v[134:137], v[2:5]
	v_mfma_f32_16x16x32_f16 v[6:9], v[166:169], v[152:155], v[6:9]
	v_mfma_f32_16x16x32_f16 v[30:33], v[188:191], v[134:137], v[30:33]
	v_mfma_f32_16x16x32_f16 v[2:5], v[176:179], v[138:141], v[2:5]
	v_mfma_f32_16x16x32_f16 v[6:9], v[176:179], v[156:159], v[6:9]
	v_mfma_f32_16x16x32_f16 v[10:13], v[180:183], v[134:137], v[10:13]
	v_mfma_f32_16x16x32_f16 v[18:21], v[180:183], v[152:155], v[18:21]
	v_mfma_f32_16x16x32_f16 v[30:33], v[198:201], v[138:141], v[30:33]
	v_mfma_f32_16x16x32_f16 v[42:45], v[188:191], v[152:155], v[42:45]
	v_mfma_f32_16x16x32_f16 v[54:57], v[202:205], v[134:137], v[54:57]
	v_mfma_f32_16x16x32_f16 v[66:69], v[202:205], v[152:155], v[66:69]
	v_mfma_f32_16x16x32_f16 v[10:13], v[184:187], v[138:141], v[10:13]
	v_mfma_f32_16x16x32_f16 v[18:21], v[184:187], v[156:159], v[18:21]
	v_mfma_f32_16x16x32_f16 v[42:45], v[198:201], v[156:159], v[42:45]
	v_mfma_f32_16x16x32_f16 v[54:57], v[206:209], v[138:141], v[54:57]
	v_mfma_f32_16x16x32_f16 v[66:69], v[206:209], v[156:159], v[66:69]
	s_barrier
	ds_read_b128 v[130:133], v161
	ds_read_b128 v[210:213], v162
	ds_read_b128 v[160:163], v163
	ds_read_b128 v[214:217], v164
	s_barrier
	s_waitcnt lgkmcnt(0)
	v_mfma_f32_16x16x32_f16 v[58:61], v[188:191], v[130:133], v[58:61]
	v_mfma_f32_16x16x32_f16 v[14:17], v[166:169], v[130:133], v[14:17]
	v_mfma_f32_16x16x32_f16 v[22:25], v[166:169], v[160:163], v[22:25]
	v_mfma_f32_16x16x32_f16 v[164:167], v[198:201], v[210:213], v[58:61]
	v_mfma_f32_16x16x32_f16 v[58:61], v[188:191], v[160:163], v[70:73]
	v_mfma_f32_16x16x32_f16 v[46:49], v[180:183], v[160:163], v[46:49]
	v_mfma_f32_16x16x32_f16 v[168:171], v[198:201], v[214:217], v[58:61]
	v_mfma_f32_16x16x32_f16 v[58:61], v[202:205], v[130:133], v[78:81]
	v_mfma_f32_16x16x32_f16 v[14:17], v[176:179], v[210:213], v[14:17]
	v_mfma_f32_16x16x32_f16 v[34:37], v[180:183], v[130:133], v[34:37]
	v_mfma_f32_16x16x32_f16 v[46:49], v[184:187], v[214:217], v[46:49]
	v_mfma_f32_16x16x32_f16 v[78:81], v[206:209], v[210:213], v[58:61]
	v_mfma_f32_16x16x32_f16 v[58:61], v[202:205], v[160:163], v[86:89]
	v_mfma_f32_16x16x32_f16 v[22:25], v[176:179], v[214:217], v[22:25]
	v_mfma_f32_16x16x32_f16 v[34:37], v[184:187], v[210:213], v[34:37]
	v_mfma_f32_16x16x32_f16 v[86:89], v[206:209], v[214:217], v[58:61]
	s_barrier
	s_nop 2
	ds_read_b128 v[58:61], v173 offset:16384
	ds_read_b128 v[70:73], v173 offset:17408
	ds_read_b128 v[174:177], v173 offset:18432
	ds_read_b128 v[178:181], v173 offset:19456
	ds_read_b128 v[182:185], v173 offset:20480
	ds_read_b128 v[186:189], v173 offset:21504
	ds_read_b128 v[190:193], v173 offset:22528
	ds_read_b128 v[198:201], v173 offset:23552
	s_waitcnt vmcnt(4)
	s_barrier
	s_waitcnt lgkmcnt(0)
	v_mfma_f32_16x16x32_f16 v[26:29], v[58:61], v[134:137], v[26:29]
	v_mfma_f32_16x16x32_f16 v[26:29], v[70:73], v[138:141], v[26:29]
	v_mfma_f32_16x16x32_f16 v[38:41], v[58:61], v[152:155], v[38:41]
	v_mfma_f32_16x16x32_f16 v[50:53], v[174:177], v[134:137], v[50:53]
	v_mfma_f32_16x16x32_f16 v[62:65], v[174:177], v[152:155], v[62:65]
	v_mfma_f32_16x16x32_f16 v[74:77], v[182:185], v[134:137], v[74:77]
	v_mfma_f32_16x16x32_f16 v[82:85], v[182:185], v[152:155], v[82:85]
	v_mfma_f32_16x16x32_f16 v[90:93], v[190:193], v[134:137], v[90:93]
	v_mfma_f32_16x16x32_f16 v[94:97], v[190:193], v[152:155], v[94:97]
	v_mfma_f32_16x16x32_f16 v[38:41], v[70:73], v[156:159], v[38:41]
	v_mfma_f32_16x16x32_f16 v[50:53], v[178:181], v[138:141], v[50:53]
	v_mfma_f32_16x16x32_f16 v[62:65], v[178:181], v[156:159], v[62:65]
	v_mfma_f32_16x16x32_f16 v[74:77], v[186:189], v[138:141], v[74:77]
	v_mfma_f32_16x16x32_f16 v[82:85], v[186:189], v[156:159], v[82:85]
	v_mfma_f32_16x16x32_f16 v[90:93], v[198:201], v[138:141], v[90:93]
	v_mfma_f32_16x16x32_f16 v[94:97], v[198:201], v[156:159], v[94:97]
	v_mfma_f32_16x16x32_f16 v[98:101], v[58:61], v[130:133], v[98:101]
	v_mfma_f32_16x16x32_f16 v[58:61], v[58:61], v[160:163], v[102:105]
	v_mfma_f32_16x16x32_f16 v[102:105], v[70:73], v[214:217], v[58:61]
	v_mfma_f32_16x16x32_f16 v[58:61], v[174:177], v[130:133], v[106:109]
	v_mfma_f32_16x16x32_f16 v[106:109], v[178:181], v[210:213], v[58:61]
	v_mfma_f32_16x16x32_f16 v[58:61], v[174:177], v[160:163], v[110:113]
	v_mfma_f32_16x16x32_f16 v[202:205], v[178:181], v[214:217], v[58:61]
	v_mfma_f32_16x16x32_f16 v[58:61], v[182:185], v[130:133], v[114:117]
	v_mfma_f32_16x16x32_f16 v[206:209], v[186:189], v[210:213], v[58:61]
	v_mfma_f32_16x16x32_f16 v[58:61], v[182:185], v[160:163], v[118:121]
	v_mfma_f32_16x16x32_f16 v[218:221], v[186:189], v[214:217], v[58:61]
	v_mfma_f32_16x16x32_f16 v[58:61], v[190:193], v[130:133], v[122:125]
	v_mfma_f32_16x16x32_f16 v[98:101], v[70:73], v[210:213], v[98:101]
	v_mfma_f32_16x16x32_f16 v[210:213], v[198:201], v[210:213], v[58:61]
	v_mfma_f32_16x16x32_f16 v[58:61], v[190:193], v[160:163], v[126:129]
	v_mfma_f32_16x16x32_f16 v[198:201], v[198:201], v[214:217], v[58:61]
	s_barrier
	ds_read_b128 v[110:113], v144
	ds_read_b128 v[130:133], v145
	ds_read_b128 v[214:217], v150
	ds_read_b128 v[222:225], v151
	s_nop 0
	ds_read_b128 v[58:61], v173 offset:32768
	ds_read_b128 v[70:73], v173 offset:33792
	ds_read_b128 v[114:117], v173 offset:34816
	ds_read_b128 v[118:121], v173 offset:35840
	ds_read_b128 v[134:137], v173 offset:36864
	ds_read_b128 v[138:141], v173 offset:37888
	ds_read_b128 v[178:181], v173 offset:38912
	ds_read_b128 v[226:229], v173 offset:39936
	s_waitcnt vmcnt(2)
	s_barrier
	s_waitcnt lgkmcnt(0)
	v_mfma_f32_16x16x32_f16 v[2:5], v[58:61], v[110:113], v[2:5]
	v_mfma_f32_16x16x32_f16 v[190:193], v[70:73], v[130:133], v[2:5]
	v_mfma_f32_16x16x32_f16 v[2:5], v[58:61], v[214:217], v[6:9]
	v_mfma_f32_16x16x32_f16 v[158:161], v[70:73], v[222:225], v[2:5]
	v_mfma_f32_16x16x32_f16 v[2:5], v[114:117], v[110:113], v[10:13]
	v_mfma_f32_16x16x32_f16 v[186:189], v[118:121], v[130:133], v[2:5]
	v_mfma_f32_16x16x32_f16 v[2:5], v[114:117], v[214:217], v[18:21]
	v_mfma_f32_16x16x32_f16 v[154:157], v[118:121], v[222:225], v[2:5]
	v_mfma_f32_16x16x32_f16 v[2:5], v[134:137], v[110:113], v[30:33]
	v_mfma_f32_16x16x32_f16 v[182:185], v[138:141], v[130:133], v[2:5]
	v_mfma_f32_16x16x32_f16 v[2:5], v[134:137], v[214:217], v[42:45]
	v_mfma_f32_16x16x32_f16 v[150:153], v[138:141], v[222:225], v[2:5]
	v_mfma_f32_16x16x32_f16 v[2:5], v[178:181], v[110:113], v[54:57]
	v_mfma_f32_16x16x32_f16 v[174:177], v[226:229], v[130:133], v[2:5]
	v_mfma_f32_16x16x32_f16 v[2:5], v[178:181], v[214:217], v[66:69]
	v_mfma_f32_16x16x32_f16 v[142:145], v[226:229], v[222:225], v[2:5]
	s_barrier
	s_nop 4
	ds_read_b128 v[2:5], v146
	ds_read_b128 v[10:13], v147
	ds_read_b128 v[18:21], v148
	ds_read_b128 v[42:45], v149
	s_waitcnt vmcnt(0)
	s_barrier
	s_waitcnt lgkmcnt(0)
	v_mfma_f32_16x16x32_f16 v[6:9], v[58:61], v[2:5], v[14:17]
	v_mfma_f32_16x16x32_f16 v[126:129], v[70:73], v[10:13], v[6:9]
	v_mfma_f32_16x16x32_f16 v[6:9], v[58:61], v[18:21], v[22:25]
	v_mfma_f32_16x16x32_f16 v[70:73], v[70:73], v[42:45], v[6:9]
	v_mfma_f32_16x16x32_f16 v[6:9], v[114:117], v[2:5], v[34:37]
	v_mfma_f32_16x16x32_f16 v[122:125], v[118:121], v[10:13], v[6:9]
	v_mfma_f32_16x16x32_f16 v[6:9], v[114:117], v[18:21], v[46:49]
	v_mfma_f32_16x16x32_f16 v[58:61], v[118:121], v[42:45], v[6:9]
	v_mfma_f32_16x16x32_f16 v[6:9], v[134:137], v[2:5], v[164:167]
	v_mfma_f32_16x16x32_f16 v[118:121], v[138:141], v[10:13], v[6:9]
	v_mfma_f32_16x16x32_f16 v[6:9], v[134:137], v[18:21], v[168:171]
	v_mfma_f32_16x16x32_f16 v[46:49], v[138:141], v[42:45], v[6:9]
	v_mfma_f32_16x16x32_f16 v[6:9], v[178:181], v[2:5], v[78:81]
	v_mfma_f32_16x16x32_f16 v[114:117], v[226:229], v[10:13], v[6:9]
	v_mfma_f32_16x16x32_f16 v[6:9], v[178:181], v[18:21], v[86:89]
	v_mfma_f32_16x16x32_f16 v[30:33], v[226:229], v[42:45], v[6:9]
	s_barrier
	s_nop 4
	ds_read_b128 v[6:9], v173 offset:49152
	ds_read_b128 v[14:17], v173 offset:50176
	ds_read_b128 v[22:25], v173 offset:51200
	ds_read_b128 v[34:37], v173 offset:52224
	ds_read_b128 v[54:57], v173 offset:53248
	ds_read_b128 v[66:69], v173 offset:54272
	ds_read_b128 v[78:81], v173 offset:55296
	ds_read_b128 v[86:89], v173 offset:56320
	s_barrier
	s_waitcnt lgkmcnt(0)
	v_mfma_f32_16x16x32_f16 v[26:29], v[6:9], v[110:113], v[26:29]
	v_mfma_f32_16x16x32_f16 v[178:181], v[14:17], v[130:133], v[26:29]
	v_mfma_f32_16x16x32_f16 v[26:29], v[6:9], v[214:217], v[38:41]
	v_mfma_f32_16x16x32_f16 v[146:149], v[14:17], v[222:225], v[26:29]
	v_mfma_f32_16x16x32_f16 v[26:29], v[22:25], v[110:113], v[50:53]
	v_mfma_f32_16x16x32_f16 v[170:173], v[34:37], v[130:133], v[26:29]
	v_mfma_f32_16x16x32_f16 v[26:29], v[22:25], v[214:217], v[62:65]
	v_mfma_f32_16x16x32_f16 v[138:141], v[34:37], v[222:225], v[26:29]
	v_mfma_f32_16x16x32_f16 v[26:29], v[54:57], v[110:113], v[74:77]
	v_mfma_f32_16x16x32_f16 v[166:169], v[66:69], v[130:133], v[26:29]
	v_mfma_f32_16x16x32_f16 v[26:29], v[54:57], v[214:217], v[82:85]
	v_mfma_f32_16x16x32_f16 v[134:137], v[66:69], v[222:225], v[26:29]
	v_mfma_f32_16x16x32_f16 v[26:29], v[78:81], v[110:113], v[90:93]
	v_mfma_f32_16x16x32_f16 v[162:165], v[86:89], v[130:133], v[26:29]
	v_mfma_f32_16x16x32_f16 v[26:29], v[78:81], v[214:217], v[94:97]
	v_mfma_f32_16x16x32_f16 v[130:133], v[86:89], v[222:225], v[26:29]
	v_mfma_f32_16x16x32_f16 v[26:29], v[6:9], v[2:5], v[98:101]
	v_mfma_f32_16x16x32_f16 v[6:9], v[6:9], v[18:21], v[102:105]
	v_mfma_f32_16x16x32_f16 v[110:113], v[14:17], v[10:13], v[26:29]
	v_mfma_f32_16x16x32_f16 v[26:29], v[14:17], v[42:45], v[6:9]
	v_mfma_f32_16x16x32_f16 v[6:9], v[22:25], v[2:5], v[106:109]
	v_mfma_f32_16x16x32_f16 v[106:109], v[34:37], v[10:13], v[6:9]
	v_mfma_f32_16x16x32_f16 v[6:9], v[22:25], v[18:21], v[202:205]
	v_mfma_f32_16x16x32_f16 v[14:17], v[34:37], v[42:45], v[6:9]
	v_mfma_f32_16x16x32_f16 v[6:9], v[54:57], v[2:5], v[206:209]
	v_mfma_f32_16x16x32_f16 v[2:5], v[78:81], v[2:5], v[210:213]
	v_mfma_f32_16x16x32_f16 v[102:105], v[66:69], v[10:13], v[6:9]
	v_mfma_f32_16x16x32_f16 v[6:9], v[54:57], v[18:21], v[218:221]
	v_mfma_f32_16x16x32_f16 v[98:101], v[86:89], v[10:13], v[2:5]
	v_mfma_f32_16x16x32_f16 v[2:5], v[78:81], v[18:21], v[198:201]
	v_mfma_f32_16x16x32_f16 v[6:9], v[66:69], v[42:45], v[6:9]
	v_mfma_f32_16x16x32_f16 v[2:5], v[86:89], v[42:45], v[2:5]
	s_cmpk_gt_u32 s54, 0xff
	s_barrier
	s_cbranch_scc1 .LBB9_34
	s_barrier
	s_branch .LBB9_34

.LBB10_12:
	ds_read_b128 v[182:185], v171
	ds_read_b128 v[186:189], v173
	ds_read_b128 v[190:193], v174
	ds_read_b128 v[194:197], v175
	v_add_u32_e32 v177, 0xc000, v148
	v_lshl_add_u64 v[246:247], v[136:137], 0, s[44:45]
	v_add_u32_e32 v176, s63, v170
	ds_read_b128 v[198:201], v176
	ds_read_b128 v[202:205], v176 offset:1024
	ds_read_b128 v[206:209], v176 offset:2048
	ds_read_b128 v[210:213], v176 offset:3072
	ds_read_b128 v[214:217], v176 offset:4096
	ds_read_b128 v[218:221], v176 offset:5120
	ds_read_b128 v[222:225], v176 offset:6144
	ds_read_b128 v[226:229], v176 offset:7168
	s_mov_b32 m0, s70
	v_lshl_add_u64 v[178:179], v[246:247], 0, s[28:29]
	global_load_lds_dwordx4 v[178:179], off
	v_add_u32_e32 v178, 0xe000, v148
	v_lshl_add_u64 v[248:249], v[134:135], 0, s[44:45]
	s_mov_b32 m0, s71
	v_lshl_add_u64 v[230:231], v[248:249], 0, s[28:29]
	global_load_lds_dwordx4 v[230:231], off
	s_waitcnt lgkmcnt(8)
	s_barrier
	s_waitcnt lgkmcnt(0)
	v_mfma_f32_16x16x32_f16 v[126:129], v[198:201], v[182:185], v[126:129]
	v_mfma_f32_16x16x32_f16 v[122:125], v[198:201], v[190:193], v[122:125]
	v_mfma_f32_16x16x32_f16 v[118:121], v[206:209], v[182:185], v[118:121]
	v_mfma_f32_16x16x32_f16 v[114:117], v[206:209], v[190:193], v[114:117]
	v_mfma_f32_16x16x32_f16 v[110:113], v[214:217], v[182:185], v[110:113]
	v_mfma_f32_16x16x32_f16 v[106:109], v[214:217], v[190:193], v[106:109]
	v_mfma_f32_16x16x32_f16 v[102:105], v[222:225], v[182:185], v[102:105]
	v_mfma_f32_16x16x32_f16 v[98:101], v[222:225], v[190:193], v[98:101]
	v_mfma_f32_16x16x32_f16 v[126:129], v[202:205], v[186:189], v[126:129]
	v_mfma_f32_16x16x32_f16 v[122:125], v[202:205], v[194:197], v[122:125]
	v_mfma_f32_16x16x32_f16 v[118:121], v[210:213], v[186:189], v[118:121]
	v_mfma_f32_16x16x32_f16 v[114:117], v[210:213], v[194:197], v[114:117]
	v_mfma_f32_16x16x32_f16 v[110:113], v[218:221], v[186:189], v[110:113]
	v_mfma_f32_16x16x32_f16 v[106:109], v[218:221], v[194:197], v[106:109]
	v_mfma_f32_16x16x32_f16 v[102:105], v[226:229], v[186:189], v[102:105]
	v_mfma_f32_16x16x32_f16 v[98:101], v[226:229], v[194:197], v[98:101]
	s_barrier
	v_lshl_add_u64 v[250:251], v[140:141], 0, s[44:45]
	v_lshl_add_u64 v[252:253], v[250:251], 0, s[30:31]
	s_mov_b32 m0, s72
	ds_read_b128 v[230:233], v162
	ds_read_b128 v[234:237], v163
	ds_read_b128 v[238:241], v164
	ds_read_b128 v[242:245], v165
	global_load_lds_dwordx4 v[252:253], off
	v_lshl_add_u64 v[252:253], v[138:139], 0, s[44:45]
	s_mov_b32 m0, s73
	v_lshl_add_u64 v[254:255], v[252:253], 0, s[30:31]
	global_load_lds_dwordx4 v[254:255], off
	s_barrier
	s_waitcnt lgkmcnt(0)
	v_mfma_f32_16x16x32_f16 v[94:97], v[198:201], v[230:233], v[94:97]
	v_mfma_f32_16x16x32_f16 v[90:93], v[198:201], v[238:241], v[90:93]
	v_mfma_f32_16x16x32_f16 v[86:89], v[206:209], v[230:233], v[86:89]
	v_mfma_f32_16x16x32_f16 v[82:85], v[206:209], v[238:241], v[82:85]
	v_mfma_f32_16x16x32_f16 v[78:81], v[214:217], v[230:233], v[78:81]
	v_mfma_f32_16x16x32_f16 v[74:77], v[214:217], v[238:241], v[74:77]
	v_mfma_f32_16x16x32_f16 v[70:73], v[222:225], v[230:233], v[70:73]
	v_mfma_f32_16x16x32_f16 v[66:69], v[222:225], v[238:241], v[66:69]
	v_mfma_f32_16x16x32_f16 v[94:97], v[202:205], v[234:237], v[94:97]
	v_mfma_f32_16x16x32_f16 v[90:93], v[202:205], v[242:245], v[90:93]
	v_mfma_f32_16x16x32_f16 v[86:89], v[210:213], v[234:237], v[86:89]
	v_mfma_f32_16x16x32_f16 v[82:85], v[210:213], v[242:245], v[82:85]
	v_mfma_f32_16x16x32_f16 v[78:81], v[218:221], v[234:237], v[78:81]
	v_mfma_f32_16x16x32_f16 v[74:77], v[218:221], v[242:245], v[74:77]
	v_mfma_f32_16x16x32_f16 v[70:73], v[226:229], v[234:237], v[70:73]
	v_mfma_f32_16x16x32_f16 v[66:69], v[226:229], v[242:245], v[66:69]
	v_lshl_add_u64 v[254:255], v[246:247], 0, s[30:31]
	s_mov_b32 m0, s74
	s_barrier
	ds_read_b128 v[198:201], v176 offset:16384
	ds_read_b128 v[202:205], v176 offset:17408
	ds_read_b128 v[206:209], v176 offset:18432
	ds_read_b128 v[210:213], v176 offset:19456
	ds_read_b128 v[214:217], v176 offset:20480
	ds_read_b128 v[218:221], v176 offset:21504
	ds_read_b128 v[222:225], v176 offset:22528
	ds_read_b128 v[226:229], v176 offset:23552
	global_load_lds_dwordx4 v[254:255], off
	s_mov_b32 m0, s75
	v_lshl_add_u64 v[254:255], v[248:249], 0, s[30:31]
	global_load_lds_dwordx4 v[254:255], off
	s_barrier
	s_waitcnt lgkmcnt(0)
	v_mfma_f32_16x16x32_f16 v[62:65], v[198:201], v[182:185], v[62:65]
	v_mfma_f32_16x16x32_f16 v[58:61], v[198:201], v[190:193], v[58:61]
	v_mfma_f32_16x16x32_f16 v[54:57], v[206:209], v[182:185], v[54:57]
	v_mfma_f32_16x16x32_f16 v[50:53], v[206:209], v[190:193], v[50:53]
	v_mfma_f32_16x16x32_f16 v[46:49], v[214:217], v[182:185], v[46:49]
	v_mfma_f32_16x16x32_f16 v[42:45], v[214:217], v[190:193], v[42:45]
	v_mfma_f32_16x16x32_f16 v[38:41], v[222:225], v[182:185], v[38:41]
	v_mfma_f32_16x16x32_f16 v[34:37], v[222:225], v[190:193], v[34:37]
	v_mfma_f32_16x16x32_f16 v[62:65], v[202:205], v[186:189], v[62:65]
	v_mfma_f32_16x16x32_f16 v[58:61], v[202:205], v[194:197], v[58:61]
	v_mfma_f32_16x16x32_f16 v[54:57], v[210:213], v[186:189], v[54:57]
	v_mfma_f32_16x16x32_f16 v[50:53], v[210:213], v[194:197], v[50:53]
	v_mfma_f32_16x16x32_f16 v[46:49], v[218:221], v[186:189], v[46:49]
	v_mfma_f32_16x16x32_f16 v[42:45], v[218:221], v[194:197], v[42:45]
	v_mfma_f32_16x16x32_f16 v[38:41], v[226:229], v[186:189], v[38:41]
	v_mfma_f32_16x16x32_f16 v[34:37], v[226:229], v[194:197], v[34:37]
	s_barrier
	s_mov_b32 m0, s76
	v_lshl_add_u64 v[182:183], v[250:251], 0, s[34:35]
	global_load_lds_dwordx4 v[182:183], off
	s_mov_b32 m0, s77
	v_lshl_add_u64 v[182:183], v[252:253], 0, s[34:35]
	global_load_lds_dwordx4 v[182:183], off
	s_waitcnt vmcnt(6)
	s_barrier
	v_mfma_f32_16x16x32_f16 v[30:33], v[198:201], v[230:233], v[30:33]
	v_mfma_f32_16x16x32_f16 v[26:29], v[198:201], v[238:241], v[26:29]
	v_mfma_f32_16x16x32_f16 v[22:25], v[206:209], v[230:233], v[22:25]
	v_mfma_f32_16x16x32_f16 v[18:21], v[206:209], v[238:241], v[18:21]
	v_mfma_f32_16x16x32_f16 v[14:17], v[214:217], v[230:233], v[14:17]
	v_mfma_f32_16x16x32_f16 v[10:13], v[214:217], v[238:241], v[10:13]
	v_mfma_f32_16x16x32_f16 v[6:9], v[222:225], v[230:233], v[6:9]
	v_mfma_f32_16x16x32_f16 v[2:5], v[222:225], v[238:241], v[2:5]
	v_mfma_f32_16x16x32_f16 v[30:33], v[202:205], v[234:237], v[30:33]
	v_mfma_f32_16x16x32_f16 v[26:29], v[202:205], v[242:245], v[26:29]
	v_mfma_f32_16x16x32_f16 v[22:25], v[210:213], v[234:237], v[22:25]
	v_mfma_f32_16x16x32_f16 v[18:21], v[210:213], v[242:245], v[18:21]
	v_mfma_f32_16x16x32_f16 v[14:17], v[218:221], v[234:237], v[14:17]
	v_mfma_f32_16x16x32_f16 v[10:13], v[218:221], v[242:245], v[10:13]
	v_mfma_f32_16x16x32_f16 v[6:9], v[226:229], v[234:237], v[6:9]
	v_mfma_f32_16x16x32_f16 v[2:5], v[226:229], v[242:245], v[2:5]
	s_barrier
	ds_read_b128 v[182:185], v144
	ds_read_b128 v[186:189], v145
	ds_read_b128 v[190:193], v146
	ds_read_b128 v[194:197], v147
	ds_read_b128 v[198:201], v176 offset:32768
	ds_read_b128 v[202:205], v176 offset:33792
	ds_read_b128 v[206:209], v176 offset:34816
	ds_read_b128 v[210:213], v176 offset:35840
	ds_read_b128 v[214:217], v176 offset:36864
	ds_read_b128 v[218:221], v176 offset:37888
	ds_read_b128 v[222:225], v176 offset:38912
	ds_read_b128 v[226:229], v176 offset:39936
	s_mov_b32 m0, s78
	v_lshl_add_u64 v[230:231], v[246:247], 0, s[34:35]
	global_load_lds_dwordx4 v[230:231], off
	s_mov_b32 m0, s79
	v_lshl_add_u64 v[230:231], v[248:249], 0, s[34:35]
	global_load_lds_dwordx4 v[230:231], off
	s_waitcnt lgkmcnt(8)
	s_barrier
	s_waitcnt lgkmcnt(0)
	v_mfma_f32_16x16x32_f16 v[126:129], v[198:201], v[182:185], v[126:129]
	v_mfma_f32_16x16x32_f16 v[122:125], v[198:201], v[190:193], v[122:125]
	v_mfma_f32_16x16x32_f16 v[118:121], v[206:209], v[182:185], v[118:121]
	v_mfma_f32_16x16x32_f16 v[114:117], v[206:209], v[190:193], v[114:117]
	v_mfma_f32_16x16x32_f16 v[110:113], v[214:217], v[182:185], v[110:113]
	v_mfma_f32_16x16x32_f16 v[106:109], v[214:217], v[190:193], v[106:109]
	v_mfma_f32_16x16x32_f16 v[102:105], v[222:225], v[182:185], v[102:105]
	v_mfma_f32_16x16x32_f16 v[98:101], v[222:225], v[190:193], v[98:101]
	v_mfma_f32_16x16x32_f16 v[126:129], v[202:205], v[186:189], v[126:129]
	v_mfma_f32_16x16x32_f16 v[122:125], v[202:205], v[194:197], v[122:125]
	v_mfma_f32_16x16x32_f16 v[118:121], v[210:213], v[186:189], v[118:121]
	v_mfma_f32_16x16x32_f16 v[114:117], v[210:213], v[194:197], v[114:117]
	v_mfma_f32_16x16x32_f16 v[110:113], v[218:221], v[186:189], v[110:113]
	v_mfma_f32_16x16x32_f16 v[106:109], v[218:221], v[194:197], v[106:109]
	v_mfma_f32_16x16x32_f16 v[102:105], v[226:229], v[186:189], v[102:105]
	v_mfma_f32_16x16x32_f16 v[98:101], v[226:229], v[194:197], v[98:101]
	s_barrier
	v_lshl_add_u64 v[254:255], v[250:251], 0, s[36:37]
	s_mov_b32 m0, s80
	ds_read_b128 v[230:233], v150
	ds_read_b128 v[234:237], v151
	ds_read_b128 v[238:241], v152
	ds_read_b128 v[242:245], v153
	global_load_lds_dwordx4 v[254:255], off
	s_mov_b32 m0, s81
	v_lshl_add_u64 v[254:255], v[252:253], 0, s[36:37]
	global_load_lds_dwordx4 v[254:255], off
	s_barrier
	s_waitcnt lgkmcnt(0)
	v_mfma_f32_16x16x32_f16 v[94:97], v[198:201], v[230:233], v[94:97]
	v_mfma_f32_16x16x32_f16 v[90:93], v[198:201], v[238:241], v[90:93]
	v_mfma_f32_16x16x32_f16 v[86:89], v[206:209], v[230:233], v[86:89]
	v_mfma_f32_16x16x32_f16 v[82:85], v[206:209], v[238:241], v[82:85]
	v_mfma_f32_16x16x32_f16 v[78:81], v[214:217], v[230:233], v[78:81]
	v_mfma_f32_16x16x32_f16 v[74:77], v[214:217], v[238:241], v[74:77]
	v_mfma_f32_16x16x32_f16 v[70:73], v[222:225], v[230:233], v[70:73]
	v_mfma_f32_16x16x32_f16 v[66:69], v[222:225], v[238:241], v[66:69]
	v_mfma_f32_16x16x32_f16 v[94:97], v[202:205], v[234:237], v[94:97]
	v_mfma_f32_16x16x32_f16 v[90:93], v[202:205], v[242:245], v[90:93]
	v_mfma_f32_16x16x32_f16 v[86:89], v[210:213], v[234:237], v[86:89]
	v_mfma_f32_16x16x32_f16 v[82:85], v[210:213], v[242:245], v[82:85]
	v_mfma_f32_16x16x32_f16 v[78:81], v[218:221], v[234:237], v[78:81]
	v_mfma_f32_16x16x32_f16 v[74:77], v[218:221], v[242:245], v[74:77]
	v_mfma_f32_16x16x32_f16 v[70:73], v[226:229], v[234:237], v[70:73]
	v_mfma_f32_16x16x32_f16 v[66:69], v[226:229], v[242:245], v[66:69]
	v_lshl_add_u64 v[246:247], v[246:247], 0, s[36:37]
	s_mov_b32 m0, s82
	s_barrier
	ds_read_b128 v[198:201], v176 offset:49152
	ds_read_b128 v[202:205], v176 offset:50176
	ds_read_b128 v[206:209], v176 offset:51200
	ds_read_b128 v[210:213], v176 offset:52224
	ds_read_b128 v[214:217], v176 offset:53248
	ds_read_b128 v[218:221], v176 offset:54272
	ds_read_b128 v[222:225], v176 offset:55296
	ds_read_b128 v[226:229], v176 offset:56320
	global_load_lds_dwordx4 v[246:247], off
	s_mov_b32 m0, s83
	v_lshl_add_u64 v[246:247], v[248:249], 0, s[36:37]
	global_load_lds_dwordx4 v[246:247], off
	s_barrier
	s_waitcnt lgkmcnt(0)
	v_mfma_f32_16x16x32_f16 v[62:65], v[198:201], v[182:185], v[62:65]
	v_mfma_f32_16x16x32_f16 v[58:61], v[198:201], v[190:193], v[58:61]
	v_mfma_f32_16x16x32_f16 v[54:57], v[206:209], v[182:185], v[54:57]
	v_mfma_f32_16x16x32_f16 v[50:53], v[206:209], v[190:193], v[50:53]
	v_mfma_f32_16x16x32_f16 v[46:49], v[214:217], v[182:185], v[46:49]
	v_mfma_f32_16x16x32_f16 v[42:45], v[214:217], v[190:193], v[42:45]
	v_mfma_f32_16x16x32_f16 v[38:41], v[222:225], v[182:185], v[38:41]
	v_mfma_f32_16x16x32_f16 v[34:37], v[222:225], v[190:193], v[34:37]
	v_mfma_f32_16x16x32_f16 v[62:65], v[202:205], v[186:189], v[62:65]
	v_mfma_f32_16x16x32_f16 v[58:61], v[202:205], v[194:197], v[58:61]
	v_mfma_f32_16x16x32_f16 v[54:57], v[210:213], v[186:189], v[54:57]
	v_mfma_f32_16x16x32_f16 v[50:53], v[210:213], v[194:197], v[50:53]
	v_mfma_f32_16x16x32_f16 v[46:49], v[218:221], v[186:189], v[46:49]
	v_mfma_f32_16x16x32_f16 v[42:45], v[218:221], v[194:197], v[42:45]
	v_mfma_f32_16x16x32_f16 v[38:41], v[226:229], v[186:189], v[38:41]
	v_mfma_f32_16x16x32_f16 v[34:37], v[226:229], v[194:197], v[34:37]
	s_barrier
	s_mov_b32 m0, s84
	v_lshl_add_u64 v[182:183], v[250:251], 0, s[38:39]
	global_load_lds_dwordx4 v[182:183], off
	s_mov_b32 m0, s85
	v_lshl_add_u64 v[182:183], v[252:253], 0, s[38:39]
	global_load_lds_dwordx4 v[182:183], off
	s_waitcnt vmcnt(6)
	s_barrier
	v_mfma_f32_16x16x32_f16 v[30:33], v[198:201], v[230:233], v[30:33]
	v_mfma_f32_16x16x32_f16 v[26:29], v[198:201], v[238:241], v[26:29]
	v_mfma_f32_16x16x32_f16 v[22:25], v[206:209], v[230:233], v[22:25]
	v_mfma_f32_16x16x32_f16 v[18:21], v[206:209], v[238:241], v[18:21]
	v_mfma_f32_16x16x32_f16 v[14:17], v[214:217], v[230:233], v[14:17]
	v_mfma_f32_16x16x32_f16 v[10:13], v[214:217], v[238:241], v[10:13]
	v_mfma_f32_16x16x32_f16 v[6:9], v[222:225], v[230:233], v[6:9]
	v_mfma_f32_16x16x32_f16 v[2:5], v[222:225], v[238:241], v[2:5]
	v_mfma_f32_16x16x32_f16 v[30:33], v[202:205], v[234:237], v[30:33]
	v_mfma_f32_16x16x32_f16 v[26:29], v[202:205], v[242:245], v[26:29]
	v_mfma_f32_16x16x32_f16 v[22:25], v[210:213], v[234:237], v[22:25]
	v_mfma_f32_16x16x32_f16 v[18:21], v[210:213], v[242:245], v[18:21]
	v_mfma_f32_16x16x32_f16 v[14:17], v[218:221], v[234:237], v[14:17]
	v_mfma_f32_16x16x32_f16 v[10:13], v[218:221], v[242:245], v[10:13]
	v_mfma_f32_16x16x32_f16 v[6:9], v[226:229], v[234:237], v[6:9]
	v_mfma_f32_16x16x32_f16 v[2:5], v[226:229], v[242:245], v[2:5]
	s_add_i32 s46, s46, 2
	s_add_u32 s44, s44, 0x100
	s_addc_u32 s45, s45, 0
	s_cmp_lt_u32 s46, 28
	s_barrier
	s_cbranch_scc1 .LBB10_12
	s_add_u32 s42, s42, 0x80f80
	s_addc_u32 s43, s43, 0
	v_readfirstlane_b32 s44, v177
	v_lshl_add_u64 v[130:131], v[130:131], 1, s[42:43]
	s_mov_b32 m0, s44
	ds_read_b128 v[134:137], v171
	ds_read_b128 v[138:141], v173
	ds_read_b128 v[154:157], v174
	ds_read_b128 v[168:171], v175
	ds_read_b128 v[182:185], v176
	ds_read_b128 v[186:189], v176 offset:1024
	ds_read_b128 v[190:193], v176 offset:2048
	ds_read_b128 v[194:197], v176 offset:3072
	ds_read_b128 v[198:201], v176 offset:4096
	ds_read_b128 v[202:205], v176 offset:5120
	ds_read_b128 v[206:209], v176 offset:6144
	ds_read_b128 v[210:213], v176 offset:7168
	global_load_lds_dwordx4 v[130:131], off
	v_lshl_add_u64 v[130:131], v[132:133], 1, s[42:43]
	v_readfirstlane_b32 s42, v178
	s_mov_b32 m0, s42
	s_nop 0
	global_load_lds_dwordx4 v[130:131], off
	s_barrier
	s_waitcnt lgkmcnt(0)
	v_mfma_f32_16x16x32_f16 v[122:125], v[182:185], v[154:157], v[122:125]
	v_mfma_f32_16x16x32_f16 v[110:113], v[198:201], v[134:137], v[110:113]
	v_mfma_f32_16x16x32_f16 v[98:101], v[206:209], v[154:157], v[98:101]
	v_mfma_f32_16x16x32_f16 v[126:129], v[182:185], v[134:137], v[126:129]
	v_mfma_f32_16x16x32_f16 v[122:125], v[186:189], v[168:171], v[122:125]
	v_mfma_f32_16x16x32_f16 v[118:121], v[190:193], v[134:137], v[118:121]
	v_mfma_f32_16x16x32_f16 v[114:117], v[190:193], v[154:157], v[114:117]
	v_mfma_f32_16x16x32_f16 v[130:133], v[202:205], v[138:141], v[110:113]
	v_mfma_f32_16x16x32_f16 v[106:109], v[198:201], v[154:157], v[106:109]
	v_mfma_f32_16x16x32_f16 v[102:105], v[206:209], v[134:137], v[102:105]
	v_mfma_f32_16x16x32_f16 v[98:101], v[210:213], v[168:171], v[98:101]
	v_mfma_f32_16x16x32_f16 v[126:129], v[186:189], v[138:141], v[126:129]
	v_mfma_f32_16x16x32_f16 v[118:121], v[194:197], v[138:141], v[118:121]
	v_mfma_f32_16x16x32_f16 v[114:117], v[194:197], v[168:171], v[114:117]
	v_mfma_f32_16x16x32_f16 v[214:217], v[202:205], v[168:171], v[106:109]
	v_mfma_f32_16x16x32_f16 v[102:105], v[210:213], v[138:141], v[102:105]
	s_barrier
	ds_read_b128 v[106:109], v162
	ds_read_b128 v[110:113], v163
	ds_read_b128 v[160:163], v164
	ds_read_b128 v[218:221], v165
	s_barrier
	s_waitcnt lgkmcnt(0)
	v_mfma_f32_16x16x32_f16 v[82:85], v[190:193], v[160:163], v[82:85]
	v_mfma_f32_16x16x32_f16 v[78:81], v[198:201], v[106:109], v[78:81]
	v_mfma_f32_16x16x32_f16 v[74:77], v[198:201], v[160:163], v[74:77]
	v_mfma_f32_16x16x32_f16 v[70:73], v[206:209], v[106:109], v[70:73]
	v_mfma_f32_16x16x32_f16 v[66:69], v[206:209], v[160:163], v[66:69]
	v_mfma_f32_16x16x32_f16 v[94:97], v[182:185], v[106:109], v[94:97]
	v_mfma_f32_16x16x32_f16 v[90:93], v[182:185], v[160:163], v[90:93]
	v_mfma_f32_16x16x32_f16 v[86:89], v[190:193], v[106:109], v[86:89]
	v_mfma_f32_16x16x32_f16 v[82:85], v[194:197], v[218:221], v[82:85]
	v_mfma_f32_16x16x32_f16 v[78:81], v[202:205], v[110:113], v[78:81]
	v_mfma_f32_16x16x32_f16 v[74:77], v[202:205], v[218:221], v[74:77]
	v_mfma_f32_16x16x32_f16 v[70:73], v[210:213], v[110:113], v[70:73]
	v_mfma_f32_16x16x32_f16 v[66:69], v[210:213], v[218:221], v[66:69]
	v_mfma_f32_16x16x32_f16 v[222:225], v[186:189], v[110:113], v[94:97]
	v_mfma_f32_16x16x32_f16 v[182:185], v[186:189], v[218:221], v[90:93]
	v_mfma_f32_16x16x32_f16 v[86:89], v[194:197], v[110:113], v[86:89]
	s_barrier
	ds_read_b128 v[90:93], v176 offset:16384
	ds_read_b128 v[94:97], v176 offset:17408
	ds_read_b128 v[186:189], v176 offset:18432
	ds_read_b128 v[190:193], v176 offset:19456
	ds_read_b128 v[194:197], v176 offset:20480
	ds_read_b128 v[198:201], v176 offset:21504
	ds_read_b128 v[202:205], v176 offset:22528
	ds_read_b128 v[206:209], v176 offset:23552
	s_waitcnt vmcnt(4)
	s_barrier
	s_waitcnt lgkmcnt(0)
	v_mfma_f32_16x16x32_f16 v[46:49], v[194:197], v[134:137], v[46:49]
	v_mfma_f32_16x16x32_f16 v[42:45], v[194:197], v[154:157], v[42:45]
	v_mfma_f32_16x16x32_f16 v[38:41], v[202:205], v[134:137], v[38:41]
	v_mfma_f32_16x16x32_f16 v[34:37], v[202:205], v[154:157], v[34:37]
	v_mfma_f32_16x16x32_f16 v[62:65], v[90:93], v[134:137], v[62:65]
	v_mfma_f32_16x16x32_f16 v[58:61], v[90:93], v[154:157], v[58:61]
	v_mfma_f32_16x16x32_f16 v[54:57], v[186:189], v[134:137], v[54:57]
	v_mfma_f32_16x16x32_f16 v[50:53], v[186:189], v[154:157], v[50:53]
	v_mfma_f32_16x16x32_f16 v[46:49], v[198:201], v[138:141], v[46:49]
	v_mfma_f32_16x16x32_f16 v[42:45], v[198:201], v[168:171], v[42:45]
	v_mfma_f32_16x16x32_f16 v[38:41], v[206:209], v[138:141], v[38:41]
	v_mfma_f32_16x16x32_f16 v[34:37], v[206:209], v[168:171], v[34:37]
	v_mfma_f32_16x16x32_f16 v[210:213], v[94:97], v[138:141], v[62:65]
	v_mfma_f32_16x16x32_f16 v[226:229], v[94:97], v[168:171], v[58:61]
	v_mfma_f32_16x16x32_f16 v[230:233], v[190:193], v[138:141], v[54:57]
	v_mfma_f32_16x16x32_f16 v[234:237], v[190:193], v[168:171], v[50:53]
	v_mfma_f32_16x16x32_f16 v[2:5], v[202:205], v[160:163], v[2:5]
	v_mfma_f32_16x16x32_f16 v[30:33], v[90:93], v[106:109], v[30:33]
	v_mfma_f32_16x16x32_f16 v[26:29], v[90:93], v[160:163], v[26:29]
	v_mfma_f32_16x16x32_f16 v[22:25], v[186:189], v[106:109], v[22:25]
	v_mfma_f32_16x16x32_f16 v[18:21], v[186:189], v[160:163], v[18:21]
	v_mfma_f32_16x16x32_f16 v[14:17], v[194:197], v[106:109], v[14:17]
	v_mfma_f32_16x16x32_f16 v[10:13], v[194:197], v[160:163], v[10:13]
	v_mfma_f32_16x16x32_f16 v[6:9], v[202:205], v[106:109], v[6:9]
	v_mfma_f32_16x16x32_f16 v[2:5], v[206:209], v[218:221], v[2:5]
	v_mfma_f32_16x16x32_f16 v[138:141], v[94:97], v[110:113], v[30:33]
	v_mfma_f32_16x16x32_f16 v[168:171], v[94:97], v[218:221], v[26:29]
	v_mfma_f32_16x16x32_f16 v[238:241], v[190:193], v[110:113], v[22:25]
	v_mfma_f32_16x16x32_f16 v[186:189], v[190:193], v[218:221], v[18:21]
	v_mfma_f32_16x16x32_f16 v[190:193], v[198:201], v[110:113], v[14:17]
	v_mfma_f32_16x16x32_f16 v[194:197], v[198:201], v[218:221], v[10:13]
	v_mfma_f32_16x16x32_f16 v[198:201], v[206:209], v[110:113], v[6:9]
	s_barrier
	s_nop 0
	ds_read_b128 v[6:9], v144
	ds_read_b128 v[10:13], v145
	ds_read_b128 v[14:17], v146
	ds_read_b128 v[160:163], v147
	ds_read_b128 v[18:21], v176 offset:32768
	ds_read_b128 v[22:25], v176 offset:33792
	ds_read_b128 v[26:29], v176 offset:34816
	ds_read_b128 v[50:53], v176 offset:35840
	ds_read_b128 v[202:205], v176 offset:36864
	ds_read_b128 v[206:209], v176 offset:37888
	ds_read_b128 v[218:221], v176 offset:38912
	ds_read_b128 v[242:245], v176 offset:39936
	s_waitcnt vmcnt(2)
	s_barrier
	s_waitcnt lgkmcnt(0)
	v_mfma_f32_16x16x32_f16 v[30:33], v[18:21], v[6:9], v[126:129]
	v_mfma_f32_16x16x32_f16 v[154:157], v[22:25], v[10:13], v[30:33]
	v_mfma_f32_16x16x32_f16 v[30:33], v[18:21], v[14:17], v[122:125]
	v_mfma_f32_16x16x32_f16 v[110:113], v[22:25], v[160:163], v[30:33]
	v_mfma_f32_16x16x32_f16 v[30:33], v[26:29], v[6:9], v[118:121]
	v_mfma_f32_16x16x32_f16 v[146:149], v[50:53], v[10:13], v[30:33]
	v_mfma_f32_16x16x32_f16 v[30:33], v[26:29], v[14:17], v[114:117]
	v_mfma_f32_16x16x32_f16 v[106:109], v[50:53], v[160:163], v[30:33]
	v_mfma_f32_16x16x32_f16 v[30:33], v[202:205], v[6:9], v[130:133]
	v_mfma_f32_16x16x32_f16 v[142:145], v[206:209], v[10:13], v[30:33]
	v_mfma_f32_16x16x32_f16 v[30:33], v[202:205], v[14:17], v[214:217]
	v_mfma_f32_16x16x32_f16 v[94:97], v[206:209], v[160:163], v[30:33]
	v_mfma_f32_16x16x32_f16 v[30:33], v[218:221], v[6:9], v[102:105]
	v_mfma_f32_16x16x32_f16 v[134:137], v[242:245], v[10:13], v[30:33]
	v_mfma_f32_16x16x32_f16 v[30:33], v[218:221], v[14:17], v[98:101]
	v_mfma_f32_16x16x32_f16 v[90:93], v[242:245], v[160:163], v[30:33]
	s_barrier
	ds_read_b128 v[102:105], v150
	ds_read_b128 v[114:117], v151
	ds_read_b128 v[118:121], v152
	ds_read_b128 v[126:129], v153
	s_waitcnt vmcnt(0)
	s_barrier
	s_waitcnt lgkmcnt(0)
	v_mfma_f32_16x16x32_f16 v[30:33], v[18:21], v[102:105], v[222:225]
	v_mfma_f32_16x16x32_f16 v[18:21], v[18:21], v[118:121], v[182:185]
	v_mfma_f32_16x16x32_f16 v[62:65], v[22:25], v[114:117], v[30:33]
	v_mfma_f32_16x16x32_f16 v[30:33], v[22:25], v[126:129], v[18:21]
	v_mfma_f32_16x16x32_f16 v[18:21], v[26:29], v[102:105], v[86:89]
	v_mfma_f32_16x16x32_f16 v[58:61], v[50:53], v[114:117], v[18:21]
	v_mfma_f32_16x16x32_f16 v[18:21], v[26:29], v[118:121], v[82:85]
	v_mfma_f32_16x16x32_f16 v[26:29], v[50:53], v[126:129], v[18:21]
	v_mfma_f32_16x16x32_f16 v[18:21], v[202:205], v[102:105], v[78:81]
	v_mfma_f32_16x16x32_f16 v[54:57], v[206:209], v[114:117], v[18:21]
	v_mfma_f32_16x16x32_f16 v[18:21], v[202:205], v[118:121], v[74:77]
	v_mfma_f32_16x16x32_f16 v[22:25], v[206:209], v[126:129], v[18:21]
	v_mfma_f32_16x16x32_f16 v[18:21], v[218:221], v[102:105], v[70:73]
	v_mfma_f32_16x16x32_f16 v[50:53], v[242:245], v[114:117], v[18:21]
	v_mfma_f32_16x16x32_f16 v[18:21], v[218:221], v[118:121], v[66:69]
	v_mfma_f32_16x16x32_f16 v[18:21], v[242:245], v[126:129], v[18:21]
	s_barrier
	ds_read_b128 v[86:89], v176 offset:49152
	ds_read_b128 v[150:153], v176 offset:50176
	ds_read_b128 v[182:185], v176 offset:51200
	ds_read_b128 v[202:205], v176 offset:52224
	ds_read_b128 v[206:209], v176 offset:53248
	ds_read_b128 v[214:217], v176 offset:54272
	ds_read_b128 v[218:221], v176 offset:55296
	ds_read_b128 v[174:177], v176 offset:56320
	s_barrier
	s_waitcnt lgkmcnt(0)
	v_mfma_f32_16x16x32_f16 v[66:69], v[86:89], v[6:9], v[210:213]
	v_mfma_f32_16x16x32_f16 v[130:133], v[150:153], v[10:13], v[66:69]
	v_mfma_f32_16x16x32_f16 v[66:69], v[86:89], v[14:17], v[226:229]
	v_mfma_f32_16x16x32_f16 v[78:81], v[150:153], v[160:163], v[66:69]
	v_mfma_f32_16x16x32_f16 v[66:69], v[182:185], v[6:9], v[230:233]
	v_mfma_f32_16x16x32_f16 v[46:49], v[206:209], v[6:9], v[46:49]
	v_mfma_f32_16x16x32_f16 v[6:9], v[218:221], v[6:9], v[38:41]
	v_mfma_f32_16x16x32_f16 v[122:125], v[202:205], v[10:13], v[66:69]
	v_mfma_f32_16x16x32_f16 v[66:69], v[182:185], v[14:17], v[234:237]
	v_mfma_f32_16x16x32_f16 v[42:45], v[206:209], v[14:17], v[42:45]
	v_mfma_f32_16x16x32_f16 v[82:85], v[174:177], v[10:13], v[6:9]
	v_mfma_f32_16x16x32_f16 v[6:9], v[218:221], v[14:17], v[34:37]
	v_mfma_f32_16x16x32_f16 v[74:77], v[202:205], v[160:163], v[66:69]
	v_mfma_f32_16x16x32_f16 v[98:101], v[214:217], v[10:13], v[46:49]
	v_mfma_f32_16x16x32_f16 v[70:73], v[214:217], v[160:163], v[42:45]
	v_mfma_f32_16x16x32_f16 v[66:69], v[174:177], v[160:163], v[6:9]
	v_mfma_f32_16x16x32_f16 v[6:9], v[86:89], v[102:105], v[138:141]
	v_mfma_f32_16x16x32_f16 v[46:49], v[150:153], v[114:117], v[6:9]
	v_mfma_f32_16x16x32_f16 v[6:9], v[86:89], v[118:121], v[168:171]
	v_mfma_f32_16x16x32_f16 v[14:17], v[150:153], v[126:129], v[6:9]
	v_mfma_f32_16x16x32_f16 v[6:9], v[182:185], v[102:105], v[238:241]
	v_mfma_f32_16x16x32_f16 v[42:45], v[202:205], v[114:117], v[6:9]
	v_mfma_f32_16x16x32_f16 v[6:9], v[182:185], v[118:121], v[186:189]
	v_mfma_f32_16x16x32_f16 v[10:13], v[202:205], v[126:129], v[6:9]
	v_mfma_f32_16x16x32_f16 v[6:9], v[206:209], v[102:105], v[190:193]
	v_mfma_f32_16x16x32_f16 v[38:41], v[214:217], v[114:117], v[6:9]
	v_mfma_f32_16x16x32_f16 v[6:9], v[206:209], v[118:121], v[194:197]
	v_mfma_f32_16x16x32_f16 v[34:37], v[218:221], v[102:105], v[198:201]
	v_mfma_f32_16x16x32_f16 v[2:5], v[218:221], v[118:121], v[2:5]
	v_mfma_f32_16x16x32_f16 v[6:9], v[214:217], v[126:129], v[6:9]
	v_mfma_f32_16x16x32_f16 v[34:37], v[174:177], v[114:117], v[34:37]
	v_mfma_f32_16x16x32_f16 v[2:5], v[174:177], v[126:129], v[2:5]
	s_cmpk_gt_u32 s61, 0xff
	s_barrier
	s_cbranch_scc1 .LBB10_15
	s_barrier
